# speedup vs baseline: 1.0113x; 1.0113x over previous
.LBB0_25:
	v_mfma_f32_32x32x16_f16 v[48:63], v[80:83], v[96:99], 0
	v_add_u32_e32 v44, s8, v226
	ds_read_b128 v[32:35], v44
	ds_read_b128 v[36:39], v44 offset:4352
	v_mfma_f32_32x32x16_f16 v[64:79], v[204:207], v[96:99], 0
	s_waitcnt lgkmcnt(1)
	v_mfma_f32_32x32x16_f16 v[48:63], v[88:91], v[32:35], v[48:63]
	ds_read_b128 v[40:43], v44 offset:16
	v_mfma_f32_32x32x16_f16 v[64:79], v[84:87], v[32:35], v[64:79]
	s_waitcnt lgkmcnt(1)
	v_mfma_f32_32x32x16_f16 v[48:63], v[100:103], v[36:39], v[48:63]
	ds_read_b128 v[32:35], v44 offset:4368
	v_mfma_f32_32x32x16_f16 v[64:79], v[92:95], v[36:39], v[64:79]
	s_waitcnt lgkmcnt(1)
	v_mfma_f32_32x32x16_f16 v[48:63], v[108:111], v[40:43], v[48:63]
	ds_read_b128 v[36:39], v44 offset:32
	v_mfma_f32_32x32x16_f16 v[64:79], v[104:107], v[40:43], v[64:79]
	s_waitcnt lgkmcnt(1)
	v_mfma_f32_32x32x16_f16 v[48:63], v[116:119], v[32:35], v[48:63]
	ds_read_b128 v[40:43], v44 offset:4384
	v_mfma_f32_32x32x16_f16 v[64:79], v[112:115], v[32:35], v[64:79]
	s_waitcnt lgkmcnt(1)
	v_mfma_f32_32x32x16_f16 v[48:63], v[120:123], v[36:39], v[48:63]
	ds_read_b128 v[32:35], v44 offset:48
	v_mfma_f32_32x32x16_f16 v[64:79], v[128:131], v[36:39], v[64:79]
	s_waitcnt lgkmcnt(1)
	v_mfma_f32_32x32x16_f16 v[48:63], v[152:155], v[40:43], v[48:63]
	ds_read_b128 v[36:39], v44 offset:4400
	v_mfma_f32_32x32x16_f16 v[64:79], v[124:127], v[40:43], v[64:79]
	s_waitcnt lgkmcnt(1)
	v_mfma_f32_32x32x16_f16 v[48:63], v[136:139], v[32:35], v[48:63]
	ds_read_b128 v[40:43], v44 offset:64
	v_mfma_f32_32x32x16_f16 v[64:79], v[132:135], v[32:35], v[64:79]
	s_waitcnt lgkmcnt(1)
	v_mfma_f32_32x32x16_f16 v[48:63], v[144:147], v[36:39], v[48:63]
	ds_read_b128 v[32:35], v44 offset:4416
	v_mfma_f32_32x32x16_f16 v[64:79], v[140:143], v[36:39], v[64:79]
	s_waitcnt lgkmcnt(1)
	v_mfma_f32_32x32x16_f16 v[48:63], v[156:159], v[40:43], v[48:63]
	ds_read_b128 v[36:39], v44 offset:80
	v_mfma_f32_32x32x16_f16 v[64:79], v[148:151], v[40:43], v[64:79]
	s_waitcnt lgkmcnt(1)
	v_mfma_f32_32x32x16_f16 v[48:63], v[164:167], v[32:35], v[48:63]
	ds_read_b128 v[40:43], v44 offset:4432
	v_mfma_f32_32x32x16_f16 v[64:79], v[160:163], v[32:35], v[64:79]
	s_waitcnt lgkmcnt(1)
	v_mfma_f32_32x32x16_f16 v[48:63], v[172:175], v[36:39], v[48:63]
	ds_read_b128 v[32:35], v44 offset:96
	v_mfma_f32_32x32x16_f16 v[64:79], v[168:171], v[36:39], v[64:79]
	s_waitcnt lgkmcnt(1)
	v_mfma_f32_32x32x16_f16 v[48:63], v[180:183], v[40:43], v[48:63]
	ds_read_b128 v[36:39], v44 offset:4448
	v_mfma_f32_32x32x16_f16 v[64:79], v[176:179], v[40:43], v[64:79]
	s_waitcnt lgkmcnt(1)
	v_mfma_f32_32x32x16_f16 v[48:63], v[188:191], v[32:35], v[48:63]
	v_mfma_f32_32x32x16_f16 v[64:79], v[184:187], v[32:35], v[64:79]
	s_waitcnt lgkmcnt(0)
	v_mfma_f32_32x32x16_f16 v[48:63], v[196:199], v[36:39], v[48:63]
	v_mfma_f32_32x32x16_f16 v[64:79], v[192:195], v[36:39], v[64:79]
	s_cmp_eq_u32 s3, 3
	s_cbranch_scc0 .Lno_pre
	s_cmpk_eq_i32 s8, 0x600
	s_cbranch_scc0 .Lno_pre
	v_mul_u32_u24_e32 v100, 0x4400, v213
	v_add_u32_e32 v100, v100, v210
	global_load_dwordx4 v[104:107], v100, s[36:37]
	global_load_dwordx4 v[108:111], v100, s[36:37] offset:1024
	global_load_dwordx4 v[112:115], v100, s[36:37] offset:2048
	global_load_dwordx4 v[116:119], v100, s[36:37] offset:3072
	v_add_u32_e32 v102, 0x1000, v100
	global_load_dwordx4 v[120:123], v102, s[36:37]
	global_load_dwordx4 v[124:127], v102, s[36:37] offset:1024
	global_load_dwordx4 v[128:131], v102, s[36:37] offset:2048
	global_load_dwordx4 v[132:135], v102, s[36:37] offset:3072
	v_add_u32_e32 v102, 0x2000, v100
	global_load_dwordx4 v[136:139], v102, s[36:37]
	global_load_dwordx4 v[140:143], v102, s[36:37] offset:1024
	global_load_dwordx4 v[144:147], v102, s[36:37] offset:2048
	global_load_dwordx4 v[148:151], v102, s[36:37] offset:3072
	v_add_u32_e32 v102, 0x3000, v100
	global_load_dwordx4 v[152:155], v102, s[36:37]
	global_load_dwordx4 v[156:159], v102, s[36:37] offset:1024
	global_load_dwordx4 v[160:163], v102, s[36:37] offset:2048
	global_load_dwordx4 v[164:167], v102, s[36:37] offset:3072
	v_add_u32_e32 v102, 0x4000, v100
	global_load_dwordx4 v[168:171], v102, s[36:37]
.Lno_pre:
	s_nop 15
	s_nop 3
	v_cvt_pk_f16_f32 v38, v64, v65
	v_cvt_pk_f16_f32 v39, v66, v67
	v_and_b32 v36, s35, v38
	v_and_b32 v37, s35, v39
	v_pk_fma_f16 v238, v36, s42, v227
	v_pk_fma_f16 v239, v37, s42, v227
	v_pk_fma_f16 v238, v238, v36, s43
	v_pk_fma_f16 v239, v239, v37, s43
	s_nop 0
	v_pk_mul_f16 v238, v238, v36
	v_pk_mul_f16 v239, v239, v37
	v_exp_f16_sdwa v238, v238 dst_sel:WORD_0 dst_unused:UNUSED_PRESERVE src0_sel:WORD_0
	v_exp_f16_sdwa v239, v239 dst_sel:WORD_0 dst_unused:UNUSED_PRESERVE src0_sel:WORD_0
	v_exp_f16_sdwa v238, v238 dst_sel:WORD_1 dst_unused:UNUSED_PRESERVE src0_sel:WORD_1
	v_exp_f16_sdwa v239, v239 dst_sel:WORD_1 dst_unused:UNUSED_PRESERVE src0_sel:WORD_1
	v_pk_add_f16 v40, v38, v36
	v_pk_add_f16 v41, v39, v37
	v_pk_fma_f16 v238, v36, v238, v40 neg_lo:[1,0,0] neg_hi:[1,0,0]
	v_pk_fma_f16 v239, v37, v239, v41 neg_lo:[1,0,0] neg_hi:[1,0,0]
	v_cvt_pk_f16_f32 v38, v68, v69
	v_cvt_pk_f16_f32 v39, v70, v71
	v_and_b32 v36, s35, v38
	v_and_b32 v37, s35, v39
	v_pk_fma_f16 v240, v36, s42, v227
	v_pk_fma_f16 v241, v37, s42, v227
	v_pk_fma_f16 v240, v240, v36, s43
	v_pk_fma_f16 v241, v241, v37, s43
	v_cvt_pk_f16_f32 v243, v72, v73
	v_cvt_pk_f16_f32 v244, v74, v75
	v_and_b32 v209, s35, v243
	v_and_b32 v242, s35, v244
	v_pk_fma_f16 v68, v209, s42, v227
	v_pk_fma_f16 v69, v242, s42, v227
	v_pk_fma_f16 v68, v68, v209, s43
	v_pk_fma_f16 v69, v69, v242, s43
	v_cvt_pk_f16_f32 v74, v76, v77
	v_cvt_pk_f16_f32 v75, v78, v79
	v_and_b32 v72, s35, v74
	v_and_b32 v73, s35, v75
	v_pk_fma_f16 v70, v72, s42, v227
	v_pk_fma_f16 v71, v73, s42, v227
	v_pk_fma_f16 v70, v70, v72, s43
	v_pk_fma_f16 v71, v71, v73, s43
	s_cmp_eq_u32 s8, 0
	v_pk_mul_f16 v240, v240, v36
	v_pk_mul_f16 v241, v241, v37
	v_exp_f16_sdwa v240, v240 dst_sel:WORD_0 dst_unused:UNUSED_PRESERVE src0_sel:WORD_0
	v_exp_f16_sdwa v241, v241 dst_sel:WORD_0 dst_unused:UNUSED_PRESERVE src0_sel:WORD_0
	v_exp_f16_sdwa v240, v240 dst_sel:WORD_1 dst_unused:UNUSED_PRESERVE src0_sel:WORD_1
	v_exp_f16_sdwa v241, v241 dst_sel:WORD_1 dst_unused:UNUSED_PRESERVE src0_sel:WORD_1
	v_pk_add_f16 v40, v38, v36
	v_pk_add_f16 v41, v39, v37
	v_pk_fma_f16 v240, v36, v240, v40 neg_lo:[1,0,0] neg_hi:[1,0,0]
	v_pk_fma_f16 v241, v37, v241, v41 neg_lo:[1,0,0] neg_hi:[1,0,0]
	v_pk_mul_f16 v68, v68, v209
	v_pk_mul_f16 v69, v69, v242
	v_exp_f16_sdwa v68, v68 dst_sel:WORD_0 dst_unused:UNUSED_PRESERVE src0_sel:WORD_0
	v_exp_f16_sdwa v69, v69 dst_sel:WORD_0 dst_unused:UNUSED_PRESERVE src0_sel:WORD_0
	v_exp_f16_sdwa v68, v68 dst_sel:WORD_1 dst_unused:UNUSED_PRESERVE src0_sel:WORD_1
	v_exp_f16_sdwa v69, v69 dst_sel:WORD_1 dst_unused:UNUSED_PRESERVE src0_sel:WORD_1
	v_pk_add_f16 v76, v243, v209
	v_pk_add_f16 v77, v244, v242
	v_pk_fma_f16 v68, v209, v68, v76 neg_lo:[1,0,0] neg_hi:[1,0,0]
	v_pk_fma_f16 v69, v242, v69, v77 neg_lo:[1,0,0] neg_hi:[1,0,0]
	v_pk_mul_f16 v70, v70, v72
	v_pk_mul_f16 v71, v71, v73
	v_exp_f16_sdwa v70, v70 dst_sel:WORD_0 dst_unused:UNUSED_PRESERVE src0_sel:WORD_0
	v_exp_f16_sdwa v71, v71 dst_sel:WORD_0 dst_unused:UNUSED_PRESERVE src0_sel:WORD_0
	v_exp_f16_sdwa v70, v70 dst_sel:WORD_1 dst_unused:UNUSED_PRESERVE src0_sel:WORD_1
	v_exp_f16_sdwa v71, v71 dst_sel:WORD_1 dst_unused:UNUSED_PRESERVE src0_sel:WORD_1
	v_pk_add_f16 v76, v74, v72
	v_pk_add_f16 v77, v75, v73
	v_pk_fma_f16 v70, v72, v70, v76 neg_lo:[1,0,0] neg_hi:[1,0,0]
	v_pk_fma_f16 v71, v73, v71, v77 neg_lo:[1,0,0] neg_hi:[1,0,0]
	v_cvt_pk_f16_f32 v74, v48, v49
	v_cvt_pk_f16_f32 v75, v50, v51
	v_and_b32 v72, s35, v74
	v_and_b32 v73, s35, v75
	v_pk_fma_f16 v64, v72, s42, v227
	v_pk_fma_f16 v65, v73, s42, v227
	v_pk_fma_f16 v64, v64, v72, s43
	v_pk_fma_f16 v65, v65, v73, s43
	v_cvt_pk_f16_f32 v78, v52, v53
	v_cvt_pk_f16_f32 v79, v54, v55
	v_and_b32 v76, s35, v78
	v_and_b32 v77, s35, v79
	v_pk_fma_f16 v66, v76, s42, v227
	v_pk_fma_f16 v67, v77, s42, v227
	v_pk_fma_f16 v66, v66, v76, s43
	v_pk_fma_f16 v67, v67, v77, s43
	v_pk_mul_f16 v64, v64, v72
	v_pk_mul_f16 v65, v65, v73
	v_exp_f16_sdwa v64, v64 dst_sel:WORD_0 dst_unused:UNUSED_PRESERVE src0_sel:WORD_0
	v_exp_f16_sdwa v65, v65 dst_sel:WORD_0 dst_unused:UNUSED_PRESERVE src0_sel:WORD_0
	v_exp_f16_sdwa v64, v64 dst_sel:WORD_1 dst_unused:UNUSED_PRESERVE src0_sel:WORD_1
	v_exp_f16_sdwa v65, v65 dst_sel:WORD_1 dst_unused:UNUSED_PRESERVE src0_sel:WORD_1
	v_pk_add_f16 v209, v74, v72
	v_pk_add_f16 v242, v75, v73
	v_pk_fma_f16 v64, v72, v64, v209 neg_lo:[1,0,0] neg_hi:[1,0,0]
	v_pk_fma_f16 v65, v73, v65, v242 neg_lo:[1,0,0] neg_hi:[1,0,0]
	v_pk_mul_f16 v66, v66, v76
	v_pk_mul_f16 v67, v67, v77
	v_exp_f16_sdwa v66, v66 dst_sel:WORD_0 dst_unused:UNUSED_PRESERVE src0_sel:WORD_0
	v_exp_f16_sdwa v67, v67 dst_sel:WORD_0 dst_unused:UNUSED_PRESERVE src0_sel:WORD_0
	v_exp_f16_sdwa v66, v66 dst_sel:WORD_1 dst_unused:UNUSED_PRESERVE src0_sel:WORD_1
	v_exp_f16_sdwa v67, v67 dst_sel:WORD_1 dst_unused:UNUSED_PRESERVE src0_sel:WORD_1
	v_pk_add_f16 v72, v78, v76
	v_pk_add_f16 v73, v79, v77
	v_pk_fma_f16 v66, v76, v66, v72 neg_lo:[1,0,0] neg_hi:[1,0,0]
	v_pk_fma_f16 v67, v77, v67, v73 neg_lo:[1,0,0] neg_hi:[1,0,0]
	v_cvt_pk_f16_f32 v74, v56, v57
	v_cvt_pk_f16_f32 v75, v58, v59
	v_and_b32 v72, s35, v74
	v_and_b32 v73, s35, v75
	v_pk_fma_f16 v48, v72, s42, v227
	v_pk_fma_f16 v49, v73, s42, v227
	v_pk_fma_f16 v48, v48, v72, s43
	v_pk_fma_f16 v49, v49, v73, s43
	v_cvt_pk_f16_f32 v58, v60, v61
	v_cvt_pk_f16_f32 v59, v62, v63
	v_and_b32 v56, s35, v58
	v_and_b32 v57, s35, v59
	v_pk_fma_f16 v50, v56, s42, v227
	v_pk_fma_f16 v51, v57, s42, v227
	v_pk_fma_f16 v50, v50, v56, s43
	v_pk_fma_f16 v51, v51, v57, s43
	v_pk_mul_f16 v48, v48, v72
	v_pk_mul_f16 v49, v49, v73
	v_exp_f16_sdwa v48, v48 dst_sel:WORD_0 dst_unused:UNUSED_PRESERVE src0_sel:WORD_0
	v_exp_f16_sdwa v49, v49 dst_sel:WORD_0 dst_unused:UNUSED_PRESERVE src0_sel:WORD_0
	v_exp_f16_sdwa v48, v48 dst_sel:WORD_1 dst_unused:UNUSED_PRESERVE src0_sel:WORD_1
	v_exp_f16_sdwa v49, v49 dst_sel:WORD_1 dst_unused:UNUSED_PRESERVE src0_sel:WORD_1
	v_pk_add_f16 v62, v74, v72
	v_pk_add_f16 v63, v75, v73
	v_pk_fma_f16 v48, v72, v48, v62 neg_lo:[1,0,0] neg_hi:[1,0,0]
	v_pk_fma_f16 v49, v73, v49, v63 neg_lo:[1,0,0] neg_hi:[1,0,0]
	v_pk_mul_f16 v50, v50, v56
	v_pk_mul_f16 v51, v51, v57
	v_exp_f16_sdwa v50, v50 dst_sel:WORD_0 dst_unused:UNUSED_PRESERVE src0_sel:WORD_0
	v_exp_f16_sdwa v51, v51 dst_sel:WORD_0 dst_unused:UNUSED_PRESERVE src0_sel:WORD_0
	v_exp_f16_sdwa v50, v50 dst_sel:WORD_1 dst_unused:UNUSED_PRESERVE src0_sel:WORD_1
	v_exp_f16_sdwa v51, v51 dst_sel:WORD_1 dst_unused:UNUSED_PRESERVE src0_sel:WORD_1
	v_pk_add_f16 v62, v58, v56
	v_pk_add_f16 v63, v59, v57
	v_pk_fma_f16 v50, v56, v50, v62 neg_lo:[1,0,0] neg_hi:[1,0,0]
	v_pk_fma_f16 v51, v57, v51, v63 neg_lo:[1,0,0] neg_hi:[1,0,0]
	ds_write2_b64 v246, v[238:239], v[240:241] offset0:136 offset1:138
	ds_write2_b64 v246, v[64:65], v[66:67] offset0:144 offset1:146
	ds_write2_b64 v246, v[68:69], v[70:71] offset0:140 offset1:142
	ds_write2_b64 v246, v[48:49], v[50:51] offset0:148 offset1:150
	ds_read2_b64 v[24:27], v249 offset1:1
	ds_read2_b64 v[28:31], v249 offset0:8 offset1:9
	ds_read2_b64 v[40:43], v250 offset1:1
	ds_read2_b64 v[44:47], v250 offset0:8 offset1:9
	s_waitcnt lgkmcnt(2)
	v_mfma_f32_16x16x32_f16 v[32:35], v[24:27], v[16:19], 0
	v_mfma_f32_16x16x32_f16 v[32:35], v[28:31], v[20:23], v[32:35]
	s_waitcnt lgkmcnt(0)
	v_mfma_f32_16x16x32_f16 v[36:39], v[40:43], v[16:19], 0
	v_mfma_f32_16x16x32_f16 v[36:39], v[44:47], v[20:23], v[36:39]
	s_nop 7
	v_max3_f32 v52, v32, v33, v34
	v_max3_f32 v52, v52, v35, v36
	v_max3_f32 v52, v52, v37, v38
	v_max_f32_e32 v52, v52, v39
	ds_bpermute_b32 v53, v247, v52
	s_waitcnt lgkmcnt(0)
	v_max_f32_e32 v52, v52, v53
	ds_bpermute_b32 v53, v245, v52
	s_waitcnt lgkmcnt(0)
	v_max_f32_e32 v48, v52, v53
	s_cbranch_scc1 .LBB0_23
	v_add_f32_e32 v49, 0x41000000, v237
	v_cmp_gt_f32_e32 vcc, v48, v49
	s_cbranch_vccz .LBB0_24
	v_max_f32_e32 v48, v48, v48
	v_max_f32_e32 v49, v237, v237
	v_max_f32_e32 v49, v49, v48
	v_sub_f32_e32 v48, v237, v49
	v_exp_f32_e32 v48, v48
	v_mov_b32_e32 v237, v49
	v_pk_mul_f32 v[14:15], v[48:49], v[14:15] op_sel_hi:[0,1]
	v_pk_mul_f32 v[12:13], v[48:49], v[12:13] op_sel_hi:[0,1]
	v_pk_mul_f32 v[10:11], v[48:49], v[10:11] op_sel_hi:[0,1]
	v_pk_mul_f32 v[8:9], v[48:49], v[8:9] op_sel_hi:[0,1]
	v_pk_mul_f32 v[6:7], v[48:49], v[6:7] op_sel_hi:[0,1]
	v_pk_mul_f32 v[4:5], v[48:49], v[4:5] op_sel_hi:[0,1]
	v_pk_mul_f32 v[2:3], v[48:49], v[2:3] op_sel_hi:[0,1]
	v_pk_mul_f32 v[0:1], v[48:49], v[0:1] op_sel_hi:[0,1]
	v_mul_f32_e32 v236, v236, v48
	s_branch .LBB0_24

.LBB0_30:
	v_mov_b32_e32 v209, v245
	v_mul_u32_u24_e32 v101, 0x4540, v213
	v_add_u32_e32 v101, v101, v210
	v_mov_b32_e32 v253, v210
	v_add_u32_e32 v254, 0xcfc0, v210
	v_add_u32_e32 v255, 0x19f80, v210
	s_waitcnt vmcnt(0)
	ds_write_b128 v101, v[104:107]
	ds_write_b128 v101, v[108:111] offset:1024
	ds_write_b128 v101, v[112:115] offset:2048
	ds_write_b128 v101, v[116:119] offset:3072
	ds_write_b128 v101, v[120:123] offset:4096
	ds_write_b128 v101, v[124:127] offset:5120
	ds_write_b128 v101, v[128:131] offset:6144
	ds_write_b128 v101, v[132:135] offset:7168
	ds_write_b128 v101, v[136:139] offset:8192
	ds_write_b128 v101, v[140:143] offset:9216
	ds_write_b128 v101, v[144:147] offset:10240
	ds_write_b128 v101, v[148:151] offset:11264
	ds_write_b128 v101, v[152:155] offset:12288
	ds_write_b128 v101, v[156:159] offset:13312
	ds_write_b128 v101, v[160:163] offset:14336
	ds_write_b128 v101, v[164:167] offset:15360
	ds_write_b128 v101, v[168:171] offset:16384
	v_readfirstlane_b32 s0, v213
	s_cmp_lt_i32 s0, 3
	s_waitcnt lgkmcnt(0)
	s_barrier
	s_cbranch_scc0 .LBB0_33
	v_mov_b32_e32 v83, 0
	v_mov_b32_e32 v211, v83
	v_lshl_add_u64 v[156:157], s[36:37], 0, v[210:211]
	s_movk_i32 s0, 0x3000
	v_add_co_u32_e32 v68, vcc, s0, v156
	s_movk_i32 s0, 0x2000
	s_nop 0
	v_addc_co_u32_e32 v69, vcc, 0, v157, vcc
	ds_read_b128 v[0:3], v253 offset:8192
	v_add_co_u32_e32 v70, vcc, s0, v156
	s_movk_i32 s0, 0x1000
	s_nop 0
	v_addc_co_u32_e32 v71, vcc, 0, v157, vcc
	ds_read_b128 v[16:19], v253 offset:9216
	ds_read_b128 v[56:59], v253
	ds_read_b128 v[52:55], v253 offset:1024
	ds_read_b128 v[48:51], v253 offset:2048
	ds_read_b128 v[44:47], v253 offset:3072
	v_add_co_u32_e32 v20, vcc, s0, v156
	s_movk_i32 s0, 0x50
	s_nop 0
	v_addc_co_u32_e32 v21, vcc, 0, v157, vcc
	ds_read_b128 v[40:43], v253 offset:4096
	ds_read_b128 v[36:39], v253 offset:5120
	ds_read_b128 v[32:35], v253 offset:6144
	ds_read_b128 v[60:63], v253 offset:12288
	ds_read_b128 v[72:75], v253 offset:7168
	ds_read_b128 v[76:79], v253 offset:10240
	v_lshl_or_b32 v20, v213, 5, v212
	v_mov_b32_e32 v21, 0x4f
	v_cmp_gt_u32_e64 s[0:1], s0, v20
	s_lshl_b32 s2, s2, 2
	s_movk_i32 s3, 0x4000
	v_cndmask_b32_e64 v100, v21, v20, s[0:1]
	v_lshl_or_b32 v64, v100, 7, v208
	v_add_u32_e32 v127, 0x22a00, v64
	ds_read_b128 v[64:67], v127
	ds_read_b128 v[84:87], v127 offset:32
	s_mov_b32 s9, 0x66666667
	v_add_co_u32_e32 v108, vcc, s3, v156
	s_movk_i32 s10, 0x5000
	s_nop 0
	v_addc_co_u32_e32 v109, vcc, 0, v157, vcc
	v_add_co_u32_e32 v152, vcc, s10, v156
	v_lshlrev_b32_e32 v82, 1, v214
	s_nop 0
	v_addc_co_u32_e32 v153, vcc, 0, v157, vcc
	v_mov_b32_e32 v126, 0x3727c5ac
	s_mov_b32 s8, 0xf800000
	v_mov_b32_e32 v208, 0x260
	v_mov_b32_e32 v80, s26
	v_mov_b32_e32 v81, s27
	s_and_b64 s[0:1], s[4:5], s[0:1]
	s_waitcnt lgkmcnt(12)
	v_mfma_f32_32x32x16_f16 v[16:31], v[16:19], v[96:99], 0
	v_mfma_f32_32x32x16_f16 v[0:15], v[0:3], v[96:99], 0
	s_waitcnt lgkmcnt(1)
	v_mfma_f32_32x32x16_f16 v[0:15], v[56:59], v[64:67], v[0:15]
	s_waitcnt lgkmcnt(1)
	v_mfma_f32_32x32x16_f16 v[16:31], v[52:55], v[64:67], v[16:31]
	v_mul_lo_u16_e32 v52, 0xcd, v100
	v_lshrrev_b16_e32 v52, 10, v52
	v_lshlrev_b32_e32 v102, 10, v52
	v_lshrrev_b32_e32 v101, 2, v52
	v_sub_u32_e32 v103, s2, v52
	s_waitcnt lgkmcnt(0)
	v_mfma_f32_32x32x16_f16 v[0:15], v[48:51], v[84:87], v[0:15]
	ds_read_b128 v[48:51], v127 offset:64
	ds_read_b128 v[88:91], v127 offset:96
	s_waitcnt lgkmcnt(2)
	v_mfma_f32_32x32x16_f16 v[16:31], v[44:47], v[84:87], v[16:31]
	ds_read_b128 v[84:87], v253 offset:18752
	ds_read_b128 v[92:95], v253 offset:19776
	ds_read_b128 v[120:123], v253 offset:11264
	ds_read_b128 v[52:55], v253 offset:13312
	ds_read_b128 v[56:59], v253 offset:14336
	ds_read_b128 v[44:47], v253 offset:15360
	ds_read_b128 v[64:67], v253 offset:16384
	s_waitcnt lgkmcnt(8)
	v_mfma_f32_32x32x16_f16 v[0:15], v[40:43], v[48:51], v[0:15]
	v_and_b32_e32 v40, 0xc00, v102
	v_add3_u32 v40, v103, v101, v40
	v_mad_u64_u32 v[158:159], s[2:3], v40, 5, v[100:101]
	v_mul_hi_i32 v42, v158, s9
	v_lshlrev_b32_e32 v40, 6, v158
	v_ashrrev_i32_e32 v41, 31, v40
	s_waitcnt lgkmcnt(8)
	v_mfma_f32_32x32x16_f16 v[16:31], v[36:39], v[48:51], v[16:31]
	v_lshrrev_b32_e32 v38, 31, v42
	v_ashrrev_i32_e32 v39, 1, v42
	v_add_u32_e32 v159, v39, v38
	v_lshlrev_b32_e32 v68, 6, v159
	v_ashrrev_i32_e32 v69, 31, v68
	v_lshl_add_u64 v[48:49], v[68:69], 2, s[24:25]
	v_lshl_add_u64 v[36:37], v[40:41], 1, s[6:7]
	s_waitcnt lgkmcnt(7)
	v_mfma_f32_32x32x16_f16 v[0:15], v[32:35], v[88:91], v[0:15]
	v_lshl_add_u64 v[70:71], v[36:37], 0, v[82:83]
	v_lshlrev_b32_e32 v82, 2, v216
	v_lshl_add_u64 v[116:117], v[48:49], 0, v[82:83]
	global_load_dwordx4 v[32:35], v82, s[28:29]
	global_load_dwordx4 v[36:39], v82, s[28:29] offset:32
	global_load_dwordx4 v[40:43], v82, s[28:29] offset:64
	global_load_dwordx4 v[128:131], v82, s[28:29] offset:96
	v_add_u32_e32 v68, 0x40000, v68
	s_mov_b32 s6, 0xd000
	s_mov_b32 s7, 0xc000
	s_waitcnt lgkmcnt(7)
	v_mfma_f32_32x32x16_f16 v[16:31], v[72:75], v[88:91], v[16:31]
	s_nop 11
	v_add_f32_e32 v69, v0, v16
	v_add_f32_e32 v90, v1, v17
	v_add_f32_e32 v69, 0, v69
	v_add_f32_e32 v91, v2, v18
	v_add_f32_e32 v69, v90, v69
	v_add_f32_e32 v100, v3, v19
	v_add_f32_e32 v69, v91, v69
	v_add_f32_e32 v101, v4, v20
	v_add_f32_e32 v69, v100, v69
	v_add_f32_e32 v102, v5, v21
	v_add_f32_e32 v69, v101, v69
	v_pk_add_f32 v[48:49], v[6:7], v[22:23]
	v_add_f32_e32 v69, v102, v69
	v_add_f32_e32 v48, v48, v69
	v_pk_add_f32 v[50:51], v[8:9], v[24:25]
	v_add_f32_e32 v48, v49, v48
	v_add_f32_e32 v48, v50, v48
	v_pk_add_f32 v[72:73], v[10:11], v[26:27]
	v_add_f32_e32 v48, v51, v48
	v_add_f32_e32 v48, v72, v48
	v_pk_add_f32 v[74:75], v[12:13], v[28:29]
	v_add_f32_e32 v48, v73, v48
	v_add_f32_e32 v48, v74, v48
	v_pk_add_f32 v[88:89], v[14:15], v[30:31]
	v_add_f32_e32 v48, v75, v48
	v_add_f32_e32 v48, v88, v48
	v_add_f32_e32 v69, v89, v48
	ds_bpermute_b32 v72, v209, v69
	global_load_dwordx4 v[48:51], v[116:117], off
	global_load_dwordx4 v[88:91], v[116:117], off offset:32
	global_load_dwordx4 v[132:135], v[116:117], off offset:64
	global_load_dwordx4 v[136:139], v[116:117], off offset:96
	global_load_dwordx4 v[104:107], v[70:71], off
	global_load_dwordx4 v[100:103], v[70:71], off offset:32
	global_load_dwordx4 v[140:143], v82, s[28:29] offset:128
	global_load_dwordx4 v[144:147], v82, s[28:29] offset:160
	global_load_dwordx4 v[148:151], v[116:117], off offset:128
	global_load_dwordx4 v[160:163], v82, s[28:29] offset:192
	global_load_dwordx4 v[164:167], v[116:117], off offset:160
	global_load_dwordx4 v[168:171], v[116:117], off offset:192
	ds_read_b128 v[172:175], v253 offset:17728
	s_waitcnt lgkmcnt(1)
	v_add_f32_e32 v69, v69, v72
	v_mul_f32_e32 v72, 0x3c800000, v69
	v_pk_add_f32 v[124:125], v[30:31], v[72:73] op_sel_hi:[1,0] neg_lo:[0,1] neg_hi:[0,1]
	v_pk_add_f32 v[154:155], v[14:15], v[72:73] op_sel_hi:[1,0] neg_lo:[0,1] neg_hi:[0,1]
	v_pk_add_f32 v[184:185], v[28:29], v[72:73] op_sel_hi:[1,0] neg_lo:[0,1] neg_hi:[0,1]
	v_pk_add_f32 v[186:187], v[12:13], v[72:73] op_sel_hi:[1,0] neg_lo:[0,1] neg_hi:[0,1]
	v_pk_add_f32 v[188:189], v[26:27], v[72:73] op_sel_hi:[1,0] neg_lo:[0,1] neg_hi:[0,1]
	v_pk_add_f32 v[190:191], v[10:11], v[72:73] op_sel_hi:[1,0] neg_lo:[0,1] neg_hi:[0,1]
	v_pk_add_f32 v[192:193], v[24:25], v[72:73] op_sel_hi:[1,0] neg_lo:[0,1] neg_hi:[0,1]
	v_pk_add_f32 v[194:195], v[8:9], v[72:73] op_sel_hi:[1,0] neg_lo:[0,1] neg_hi:[0,1]
	v_pk_add_f32 v[196:197], v[22:23], v[72:73] op_sel_hi:[1,0] neg_lo:[0,1] neg_hi:[0,1]
	v_pk_add_f32 v[74:75], v[6:7], v[72:73] op_sel_hi:[1,0] neg_lo:[0,1] neg_hi:[0,1]
	v_pk_add_f32 v[198:199], v[20:21], v[72:73] op_sel_hi:[1,0] neg_lo:[0,1] neg_hi:[0,1]
	v_pk_add_f32 v[118:119], v[4:5], v[72:73] op_sel_hi:[1,0] neg_lo:[0,1] neg_hi:[0,1]
	v_pk_add_f32 v[200:201], v[18:19], v[72:73] op_sel_hi:[1,0] neg_lo:[0,1] neg_hi:[0,1]
	v_pk_add_f32 v[202:203], v[2:3], v[72:73] op_sel_hi:[1,0] neg_lo:[0,1] neg_hi:[0,1]
	v_pk_add_f32 v[204:205], v[16:17], v[72:73] op_sel_hi:[1,0] neg_lo:[0,1] neg_hi:[0,1]
	v_pk_add_f32 v[72:73], v[0:1], v[72:73] op_sel_hi:[1,0] neg_lo:[0,1] neg_hi:[0,1]
	global_load_dwordx4 v[112:115], v[70:71], off offset:64
	global_load_dwordx4 v[108:111], v[70:71], off offset:96
	global_load_dwordx4 v[176:179], v82, s[28:29] offset:224
	global_load_dwordx4 v[180:183], v[116:117], off offset:224
	v_fma_f32 v0, v72, v72, 0
	v_fmac_f32_e32 v0, v204, v204
	v_fmac_f32_e32 v0, v73, v73
	v_fmac_f32_e32 v0, v205, v205
	v_fmac_f32_e32 v0, v202, v202
	v_fmac_f32_e32 v0, v200, v200
	v_fmac_f32_e32 v0, v203, v203
	v_fmac_f32_e32 v0, v201, v201
	v_fmac_f32_e32 v0, v118, v118
	v_fmac_f32_e32 v0, v198, v198
	v_fmac_f32_e32 v0, v119, v119
	v_fmac_f32_e32 v0, v199, v199
	v_fmac_f32_e32 v0, v74, v74
	v_fmac_f32_e32 v0, v196, v196
	v_fmac_f32_e32 v0, v75, v75
	v_fmac_f32_e32 v0, v197, v197
	v_fmac_f32_e32 v0, v194, v194
	v_fmac_f32_e32 v0, v192, v192
	v_fmac_f32_e32 v0, v195, v195
	v_fmac_f32_e32 v0, v193, v193
	v_fmac_f32_e32 v0, v190, v190
	v_fmac_f32_e32 v0, v188, v188
	v_fmac_f32_e32 v0, v191, v191
	v_fmac_f32_e32 v0, v189, v189
	v_fmac_f32_e32 v0, v186, v186
	v_fmac_f32_e32 v0, v184, v184
	v_fmac_f32_e32 v0, v187, v187
	v_fmac_f32_e32 v0, v185, v185
	v_fmac_f32_e32 v0, v154, v154
	v_fmac_f32_e32 v0, v124, v124
	v_fmac_f32_e32 v0, v155, v155
	v_fmac_f32_e32 v0, v125, v125
	ds_bpermute_b32 v1, v209, v0
	s_waitcnt lgkmcnt(0)
	v_add_f32_e32 v0, v0, v1
	v_fmamk_f32 v0, v0, 0x3c800000, v126
	v_mul_f32_e32 v1, 0x4f800000, v0
	v_cmp_gt_f32_e32 vcc, s8, v0
	s_nop 1
	v_cndmask_b32_e32 v0, v0, v1, vcc
	v_sqrt_f32_e32 v1, v0
	s_nop 0
	v_add_u32_e32 v2, -1, v1
	v_fma_f32 v3, -v2, v1, v0
	v_cmp_ge_f32_e64 s[2:3], 0, v3
	v_add_u32_e32 v3, 1, v1
	s_nop 0
	v_cndmask_b32_e64 v2, v1, v2, s[2:3]
	v_fma_f32 v1, -v3, v1, v0
	v_cmp_lt_f32_e64 s[2:3], 0, v1
	s_nop 1
	v_cndmask_b32_e64 v1, v2, v3, s[2:3]
	v_mul_f32_e32 v2, 0x37800000, v1
	v_cndmask_b32_e32 v1, v1, v2, vcc
	v_cmp_class_f32_e32 vcc, v0, v208
	s_nop 1
	v_cndmask_b32_e32 v69, v1, v0, vcc
	v_div_scale_f32 v16, s[2:3], v69, v69, 1.0
	v_rcp_f32_e32 v206, v16
	s_waitcnt lgkmcnt(0)
	v_mfma_f32_32x32x16_f16 v[0:15], v[84:87], v[96:99], 0
	ds_read_b128 v[84:87], v127 offset:10240
	s_mov_b32 s2, 0xa000
	v_fma_f32 v17, -v16, v206, 1.0
	v_fmac_f32_e32 v206, v17, v206
	v_div_scale_f32 v17, vcc, 1.0, v69, 1.0
	v_mul_f32_e32 v70, v17, v206
	v_fma_f32 v18, -v16, v70, v17
	v_fmac_f32_e32 v70, v18, v206
	v_fma_f32 v71, -v16, v70, v17
	s_waitcnt lgkmcnt(1)
	v_mfma_f32_32x32x16_f16 v[16:31], v[92:95], v[96:99], 0
	ds_read_b128 v[92:95], v127 offset:10272
	v_div_fmas_f32 v70, v71, v206, v70
	v_div_fixup_f32 v70, v70, v69, 1.0
	v_mul_f32_e64 v210, v118, v70
	v_mul_f32_e64 v211, v119, v70
	v_pk_mul_f32 v[206:207], v[74:75], v[70:71] op_sel_hi:[1,0]
	v_pk_mul_f32 v[74:75], v[202:203], v[70:71] op_sel_hi:[1,0]
	s_waitcnt vmcnt(14) lgkmcnt(2)
	v_pk_fma_f32 v[36:37], v[210:211], v[36:37], v[88:89]
	s_waitcnt vmcnt(14) lgkmcnt(1)
	v_mfma_f32_32x32x16_f16 v[0:15], v[76:79], v[84:87], v[0:15]
	v_fma_f32 v34, v74, v34, v50
	v_fma_f32 v35, v75, v35, v51
	v_fma_f32 v38, v206, v38, v90
	v_fma_f32 v39, v207, v39, v91
	v_cvt_pk_f16_f32 v50, v36, v37
	v_pk_mul_f32 v[36:37], v[154:155], v[70:71] op_sel_hi:[1,0]
	v_cvt_pk_f16_f32 v51, v38, v39
	v_pk_mul_f32 v[38:39], v[186:187], v[70:71] op_sel_hi:[1,0]
	s_waitcnt vmcnt(12) lgkmcnt(1)
	v_pk_fma_f32 v[36:37], v[36:37], v[130:131], v[138:139]
	v_mfma_f32_32x32x16_f16 v[16:31], v[120:123], v[84:87], v[16:31]
	ds_read_b128 v[84:87], v127 offset:10336
	v_mul_f32_e64 v72, v72, v70
	v_mul_f32_e64 v73, v73, v70
	v_mul_f32_e64 v88, v184, v70
	v_mul_f32_e64 v89, v185, v70
	v_pk_fma_f32 v[32:33], v[72:73], v[32:33], v[48:49]
	v_cvt_pk_f16_f32 v49, v34, v35
	v_cvt_pk_f16_f32 v48, v32, v33
	v_pk_mul_f32 v[32:33], v[190:191], v[70:71] op_sel_hi:[1,0]
	s_waitcnt vmcnt(12) lgkmcnt(1)
	v_mfma_f32_32x32x16_f16 v[0:15], v[60:63], v[92:95], v[0:15]
	v_fma_f32 v60, v38, v128, v136
	v_fma_f32 v61, v39, v129, v137
	v_mul_f32_e64 v62, v204, v70
	v_mul_f32_e64 v63, v205, v70
	v_mul_f32_e64 v34, v194, v70
	v_mul_f32_e64 v35, v195, v70
	s_waitcnt vmcnt(7) lgkmcnt(1)
	v_pk_fma_f32 v[62:63], v[62:63], v[140:141], v[148:149]
	v_pk_fma_f32 v[40:41], v[34:35], v[40:41], v[132:133]
	v_pk_fma_f32 v[42:43], v[32:33], v[42:43], v[134:135]
	global_load_dwordx4 v[116:119], v82, s[30:31]
	global_load_dwordx4 v[72:75], v82, s[30:31] offset:32
	v_mfma_f32_32x32x16_f16 v[16:31], v[52:55], v[92:95], v[16:31]
	v_cvt_pk_f16_f32 v55, v36, v37
	ds_read_b128 v[36:39], v127 offset:10304
	v_cvt_pk_f16_f32 v54, v60, v61
	v_mul_f32_e64 v60, v200, v70
	v_mul_f32_e64 v61, v201, v70
	global_load_dwordx4 v[76:79], v82, s[30:31] offset:64
	global_load_dwordx4 v[32:35], v82, s[30:31] offset:96
	v_pk_fma_f32 v[60:61], v[60:61], v[142:143], v[150:151]
	s_waitcnt vmcnt(11) lgkmcnt(0)
	v_mfma_f32_32x32x16_f16 v[0:15], v[56:59], v[36:39], v[0:15]
	v_mul_f32_e64 v56, v196, v70
	v_mul_f32_e64 v57, v197, v70
	v_mul_f32_e64 v58, v198, v70
	v_mul_f32_e64 v59, v199, v70
	v_cvt_pk_f16_f32 v53, v42, v43
	v_cvt_pk_f16_f32 v52, v40, v41
	global_load_dwordx4 v[40:43], v82, s[30:31] offset:128
	v_mfma_f32_32x32x16_f16 v[16:31], v[44:47], v[36:39], v[16:31]
	s_waitcnt vmcnt(10) lgkmcnt(0)
	v_fma_f32 v38, v56, v146, v166
	v_fma_f32 v39, v57, v147, v167
	v_cvt_pk_f16_f32 v57, v60, v61
	v_mul_f32_e64 v60, v188, v70
	v_mul_f32_e64 v61, v189, v70
	v_cvt_pk_f16_f32 v56, v62, v63
	v_pk_mul_f32 v[62:63], v[124:125], v[70:71] op_sel_hi:[1,0]
	s_waitcnt vmcnt(9) lgkmcnt(0)
	v_pk_fma_f32 v[60:61], v[60:61], v[162:163], v[170:171]
	v_add_co_u32_e32 v170, vcc, s2, v156
	v_mfma_f32_32x32x16_f16 v[0:15], v[64:67], v[84:87], v[0:15]
	v_mul_f32_e64 v64, v192, v70
	v_mul_f32_e64 v65, v193, v70
	v_fma_f32 v36, v58, v144, v164
	v_fma_f32 v37, v59, v145, v165
	v_fma_f32 v136, v64, v160, v168
	v_fma_f32 v137, v65, v161, v169
	s_waitcnt vmcnt(5) lgkmcnt(0)
	v_pk_fma_f32 v[70:71], v[88:89], v[176:177], v[180:181]
	v_pk_fma_f32 v[62:63], v[62:63], v[178:179], v[182:183]
	v_addc_co_u32_e32 v171, vcc, 0, v157, vcc
	v_mfma_f32_32x32x16_f16 v[16:31], v[172:175], v[84:87], v[16:31]
	global_load_dwordx4 v[44:47], v82, s[30:31] offset:160
	v_cvt_pk_f16_f32 v59, v38, v39
	v_cvt_pk_f16_f32 v58, v36, v37
	global_load_dwordx4 v[36:39], v82, s[30:31] offset:192
	v_cvt_pk_f16_f32 v63, v62, v63
	v_cvt_pk_f16_f32 v62, v70, v71
	s_movk_i32 s2, 0x7000
	s_nop 4
	v_add_f32_e32 v64, v0, v16
	v_add_f32_e32 v64, 0, v64
	v_add_f32_e32 v65, v1, v17
	v_add_f32_e32 v64, v65, v64
	v_add_f32_e32 v65, v2, v18
	v_add_f32_e32 v64, v65, v64
	v_add_f32_e32 v65, v3, v19
	v_add_f32_e32 v64, v65, v64
	v_add_f32_e32 v65, v4, v20
	v_add_f32_e32 v64, v65, v64
	v_add_f32_e32 v65, v5, v21
	v_add_f32_e32 v66, v65, v64
	v_pk_add_f32 v[64:65], v[6:7], v[22:23]
	v_add_co_u32_e32 v184, vcc, s2, v156
	v_add_f32_e32 v64, v64, v66
	v_add_f32_e32 v66, v65, v64
	v_pk_add_f32 v[64:65], v[8:9], v[24:25]
	v_addc_co_u32_e32 v185, vcc, 0, v157, vcc
	v_add_f32_e32 v64, v64, v66
	v_add_f32_e32 v66, v65, v64
	v_pk_add_f32 v[64:65], v[10:11], v[26:27]
	s_movk_i32 s2, 0x6000
	v_add_f32_e32 v64, v64, v66
	v_add_f32_e32 v66, v65, v64
	v_pk_add_f32 v[64:65], v[12:13], v[28:29]
	v_add_co_u32_e32 v186, vcc, s2, v156
	v_add_f32_e32 v64, v64, v66
	v_add_f32_e32 v66, v65, v64
	v_pk_add_f32 v[64:65], v[14:15], v[30:31]
	v_addc_co_u32_e32 v187, vcc, 0, v157, vcc
	v_add_f32_e32 v64, v64, v66
	v_add_f32_e32 v69, v65, v64
	ds_bpermute_b32 v84, v209, v69
	global_load_dwordx4 v[64:67], v82, s[30:31] offset:224
	v_cvt_pk_f16_f32 v61, v60, v61
	v_cvt_pk_f16_f32 v60, v136, v137
	s_waitcnt vmcnt(8) lgkmcnt(0)
	v_add_f32_e32 v69, v69, v84
	v_mul_f32_e32 v92, 0x3c800000, v69
	v_ashrrev_i32_e32 v69, 31, v68
	v_lshl_add_u64 v[68:69], v[68:69], 2, s[24:25]
	v_lshl_add_u64 v[124:125], v[68:69], 0, v[82:83]
	global_load_dwordx4 v[140:143], v[124:125], off
	global_load_dwordx4 v[88:91], v[124:125], off offset:32
	global_load_dwordx4 v[84:87], v[124:125], off offset:64
	global_load_dwordx4 v[68:71], v[124:125], off offset:96
	v_pk_add_f32 v[180:181], v[10:11], v[92:93] op_sel_hi:[1,0] neg_lo:[0,1] neg_hi:[0,1]
	v_pk_add_f32 v[182:183], v[8:9], v[92:93] op_sel_hi:[1,0] neg_lo:[0,1] neg_hi:[0,1]
	v_pk_add_f32 v[8:9], v[2:3], v[92:93] op_sel_hi:[1,0] neg_lo:[0,1] neg_hi:[0,1]
	v_pk_add_f32 v[10:11], v[0:1], v[92:93] op_sel_hi:[1,0] neg_lo:[0,1] neg_hi:[0,1]
	ds_read_b128 v[0:3], v253 offset:37504
	v_pk_add_f32 v[178:179], v[12:13], v[92:93] op_sel_hi:[1,0] neg_lo:[0,1] neg_hi:[0,1]
	v_pk_add_f32 v[174:175], v[16:17], v[92:93] op_sel_hi:[1,0] neg_lo:[0,1] neg_hi:[0,1]
	v_fma_f32 v12, v10, v10, 0
	v_fmac_f32_e32 v12, v174, v174
	v_fmac_f32_e32 v12, v11, v11
	v_fmac_f32_e32 v12, v175, v175
	v_pk_add_f32 v[172:173], v[18:19], v[92:93] op_sel_hi:[1,0] neg_lo:[0,1] neg_hi:[0,1]
	v_fmac_f32_e32 v12, v8, v8
	ds_read_b128 v[144:147], v253 offset:20800
	ds_read_b128 v[148:151], v253 offset:22848
	v_fmac_f32_e32 v12, v172, v172
	v_fmac_f32_e32 v12, v9, v9
	v_pk_add_f32 v[4:5], v[4:5], v[92:93] op_sel_hi:[1,0] neg_lo:[0,1] neg_hi:[0,1]
	v_fmac_f32_e32 v12, v173, v173
	v_pk_add_f32 v[168:169], v[20:21], v[92:93] op_sel_hi:[1,0] neg_lo:[0,1] neg_hi:[0,1]
	v_fmac_f32_e32 v12, v4, v4
	v_fmac_f32_e32 v12, v168, v168
	v_fmac_f32_e32 v12, v5, v5
	v_pk_add_f32 v[6:7], v[6:7], v[92:93] op_sel_hi:[1,0] neg_lo:[0,1] neg_hi:[0,1]
	v_fmac_f32_e32 v12, v169, v169
	v_pk_add_f32 v[166:167], v[22:23], v[92:93] op_sel_hi:[1,0] neg_lo:[0,1] neg_hi:[0,1]
	v_fmac_f32_e32 v12, v6, v6
	v_fmac_f32_e32 v12, v166, v166
	v_fmac_f32_e32 v12, v7, v7
	v_fmac_f32_e32 v12, v167, v167
	v_pk_add_f32 v[164:165], v[24:25], v[92:93] op_sel_hi:[1,0] neg_lo:[0,1] neg_hi:[0,1]
	v_fmac_f32_e32 v12, v182, v182
	v_fmac_f32_e32 v12, v164, v164
	v_fmac_f32_e32 v12, v183, v183
	v_fmac_f32_e32 v12, v165, v165
	v_pk_add_f32 v[162:163], v[26:27], v[92:93] op_sel_hi:[1,0] neg_lo:[0,1] neg_hi:[0,1]
	v_fmac_f32_e32 v12, v180, v180
	v_fmac_f32_e32 v12, v162, v162
	v_fmac_f32_e32 v12, v181, v181
	v_fmac_f32_e32 v12, v163, v163
	v_pk_add_f32 v[160:161], v[28:29], v[92:93] op_sel_hi:[1,0] neg_lo:[0,1] neg_hi:[0,1]
	v_fmac_f32_e32 v12, v178, v178
	v_fmac_f32_e32 v12, v160, v160
	v_pk_add_f32 v[154:155], v[30:31], v[92:93] op_sel_hi:[1,0] neg_lo:[0,1] neg_hi:[0,1]
	v_pk_add_f32 v[176:177], v[14:15], v[92:93] op_sel_hi:[1,0] neg_lo:[0,1] neg_hi:[0,1]
	v_fmac_f32_e32 v12, v179, v179
	ds_read_b128 v[92:95], v253 offset:24896
	global_load_dwordx4 v[28:31], v[124:125], off offset:128
	global_load_dwordx4 v[20:23], v[124:125], off offset:160
	v_fmac_f32_e32 v12, v161, v161
	v_fmac_f32_e32 v12, v176, v176
	ds_read_b128 v[120:123], v253 offset:26944
	v_fmac_f32_e32 v12, v154, v154
	v_fmac_f32_e32 v12, v177, v177
	v_fmac_f32_e32 v12, v155, v155
	ds_bpermute_b32 v13, v209, v12
	s_waitcnt vmcnt(14) lgkmcnt(0)
	v_add_f32_e32 v12, v12, v13
	v_fmac_f32_e32 v126, 0x3c800000, v12
	v_mul_f32_e32 v12, 0x4f800000, v126
	v_cmp_gt_f32_e32 vcc, s8, v126
	s_nop 1
	v_cndmask_b32_e32 v12, v126, v12, vcc
	global_load_dwordx4 v[24:27], v[124:125], off offset:192
	global_load_dwordx4 v[16:19], v[124:125], off offset:224
	s_nop 0
	ds_read_b128 v[124:127], v253 offset:28992
	ds_read_b128 v[128:131], v253 offset:31040
	v_sqrt_f32_e32 v13, v12
	s_nop 0
	v_add_u32_e32 v14, -1, v13
	v_fma_f32 v15, -v14, v13, v12
	v_cmp_ge_f32_e64 s[2:3], 0, v15
	v_add_u32_e32 v15, 1, v13
	s_nop 0
	v_cndmask_b32_e64 v14, v13, v14, s[2:3]
	v_fma_f32 v13, -v15, v13, v12
	v_cmp_lt_f32_e64 s[2:3], 0, v13
	s_nop 1
	v_cndmask_b32_e64 v13, v14, v15, s[2:3]
	v_mul_f32_e32 v14, 0x37800000, v13
	s_mov_b32 s2, 0x8000
	v_cndmask_b32_e32 v13, v13, v14, vcc
	v_add_co_u32_e32 v188, vcc, s2, v156
	s_nop 1
	v_addc_co_u32_e32 v189, vcc, 0, v157, vcc
	v_cmp_class_f32_e32 vcc, v12, v208
	ds_read_b128 v[132:135], v253 offset:33088
	ds_read_b128 v[136:139], v253 offset:35456
	v_cndmask_b32_e32 v12, v13, v12, vcc
	v_div_scale_f32 v13, s[2:3], v12, v12, 1.0
	v_rcp_f32_e32 v14, v13
	s_mov_b32 s2, 0x9000
	s_mov_b32 s3, 0xbc90
	v_fma_f32 v15, -v13, v14, 1.0
	v_fmac_f32_e32 v14, v15, v14
	v_div_scale_f32 v15, vcc, 1.0, v12, 1.0
	v_mul_f32_e32 v82, v15, v14
	v_fma_f32 v190, -v13, v82, v15
	v_fmac_f32_e32 v82, v190, v14
	v_fma_f32 v13, -v13, v82, v15
	v_div_fmas_f32 v13, v13, v14, v82
	v_div_fixup_f32 v82, v13, v12, 1.0
	v_pk_mul_f32 v[190:191], v[6:7], v[82:83] op_sel_hi:[1,0]
	v_pk_mul_f32 v[192:193], v[4:5], v[82:83] op_sel_hi:[1,0]
	v_pk_mul_f32 v[4:5], v[8:9], v[82:83] op_sel_hi:[1,0]
	v_pk_mul_f32 v[6:7], v[10:11], v[82:83] op_sel_hi:[1,0]
	s_waitcnt vmcnt(7) lgkmcnt(4)
	v_pk_fma_f32 v[118:119], v[4:5], v[118:119], v[142:143]
	v_pk_fma_f32 v[116:117], v[6:7], v[116:117], v[140:141]
	s_waitcnt vmcnt(4) lgkmcnt(4)
	v_mfma_f32_32x32x16_f16 v[0:15], v[0:3], v[96:99], 0
	v_fma_f32 v72, v192, v72, v88
	v_fma_f32 v73, v193, v73, v89
	v_fma_f32 v74, v190, v74, v90
	v_fma_f32 v75, v191, v75, v91
	ds_read_b128 v[88:91], v253 offset:21824
	v_cvt_pk_f16_f32 v75, v74, v75
	v_cvt_pk_f16_f32 v74, v72, v73
	v_cvt_pk_f16_f32 v73, v118, v119
	v_pk_mul_f32 v[118:119], v[178:179], v[82:83] op_sel_hi:[1,0]
	s_waitcnt vmcnt(4) lgkmcnt(5)
	v_mfma_f32_32x32x16_f16 v[0:15], v[144:147], v[104:107], v[0:15]
	v_mul_f32_e64 v144, v180, v82
	v_mul_f32_e64 v145, v181, v82
	v_mul_f32_e64 v146, v182, v82
	v_mul_f32_e64 v147, v183, v82
	v_fma_f32 v144, v144, v78, v86
	v_fma_f32 v145, v145, v79, v87
	v_pk_fma_f32 v[146:147], v[146:147], v[76:77], v[84:85]
	ds_read_b128 v[84:87], v253 offset:23872
	v_add_co_u32_e32 v152, vcc, s2, v156
	s_waitcnt vmcnt(4) lgkmcnt(6)
	v_mfma_f32_32x32x16_f16 v[0:15], v[148:151], v[100:103], v[0:15]
	v_addc_co_u32_e32 v153, vcc, 0, v157, vcc
	v_fma_f32 v32, v118, v32, v68
	v_fma_f32 v33, v119, v33, v69
	v_cvt_pk_f16_f32 v69, v144, v145
	v_cvt_pk_f16_f32 v68, v146, v147
	ds_read_b128 v[144:147], v253 offset:27968
	ds_read_b128 v[148:151], v253 offset:32064
	s_waitcnt vmcnt(4) lgkmcnt(8)
	v_mfma_f32_32x32x16_f16 v[0:15], v[92:95], v[112:115], v[0:15]
	ds_read_b128 v[92:95], v253 offset:38528
	ds_read_b128 v[76:79], v253 offset:44672
	v_cvt_pk_f16_f32 v72, v116, v117
	v_mul_f32_e64 v116, v176, v82
	v_mul_f32_e64 v117, v177, v82
	v_pk_mul_f32 v[118:119], v[174:175], v[82:83] op_sel_hi:[1,0]
	v_pk_fma_f32 v[34:35], v[116:117], v[34:35], v[70:71]
	v_pk_mul_f32 v[116:117], v[172:173], v[82:83] op_sel_hi:[1,0]
	s_waitcnt vmcnt(2) lgkmcnt(10)
	v_mfma_f32_32x32x16_f16 v[0:15], v[120:123], v[108:111], v[0:15]
	ds_read_b128 v[120:123], v253 offset:30016
	v_fma_f32 v28, v118, v40, v28
	v_fma_f32 v29, v119, v41, v29
	v_fma_f32 v30, v116, v42, v30
	v_fma_f32 v31, v117, v43, v31
	v_cvt_pk_f16_f32 v40, v28, v29
	v_cvt_pk_f16_f32 v41, v30, v31
	v_pk_mul_f32 v[28:29], v[162:163], v[82:83] op_sel_hi:[1,0]
	v_pk_mul_f32 v[30:31], v[164:165], v[82:83] op_sel_hi:[1,0]
	s_waitcnt vmcnt(0) lgkmcnt(10)
	v_mfma_f32_32x32x16_f16 v[0:15], v[124:127], v[48:51], v[0:15]
	v_fma_f32 v24, v30, v36, v24
	v_fma_f32 v25, v31, v37, v25
	v_fma_f32 v26, v28, v38, v26
	v_fma_f32 v27, v29, v39, v27
	ds_read_b128 v[36:39], v253 offset:34112
	v_cvt_pk_f16_f32 v71, v34, v35
	v_cvt_pk_f16_f32 v70, v32, v33
	v_pk_mul_f32 v[32:33], v[166:167], v[82:83] op_sel_hi:[1,0]
	v_pk_mul_f32 v[34:35], v[168:169], v[82:83] op_sel_hi:[1,0]
	s_waitcnt vmcnt(0) lgkmcnt(10)
	v_mfma_f32_32x32x16_f16 v[0:15], v[128:131], v[52:55], v[0:15]
	ds_read_b128 v[126:129], v253 offset:25920
	v_fma_f32 v20, v34, v44, v20
	v_fma_f32 v21, v35, v45, v21
	v_fma_f32 v22, v32, v46, v22
	v_fma_f32 v23, v33, v47, v23
	v_cvt_pk_f16_f32 v42, v20, v21
	v_cvt_pk_f16_f32 v43, v22, v23
	v_pk_mul_f32 v[20:21], v[154:155], v[82:83] op_sel_hi:[1,0]
	v_pk_mul_f32 v[22:23], v[160:161], v[82:83] op_sel_hi:[1,0]
	s_waitcnt vmcnt(0) lgkmcnt(10)
	v_mfma_f32_32x32x16_f16 v[0:15], v[132:135], v[56:59], v[0:15]
	v_fma_f32 v16, v22, v64, v16
	v_fma_f32 v17, v23, v65, v17
	v_fma_f32 v18, v20, v66, v18
	v_fma_f32 v19, v21, v67, v19
	ds_read_b128 v[64:67], v253 offset:36480
	s_mov_b32 s2, 0xa714
	v_mov_b32_e32 v164, 0xb7d0
	v_cvt_pk_f16_f32 v34, v16, v17
	v_cvt_pk_f16_f32 v35, v18, v19
	s_waitcnt vmcnt(0) lgkmcnt(10)
	v_mfma_f32_32x32x16_f16 v[0:15], v[136:139], v[60:63], v[0:15]
	v_cvt_pk_f16_f32 v33, v26, v27
	v_cvt_pk_f16_f32 v32, v24, v25
	ds_read_b128 v[132:135], v253 offset:39552
	v_add_co_u32_e32 v136, vcc, s6, v156
	ds_read_b128 v[140:143], v253 offset:41600
	ds_read_b128 v[44:47], v253 offset:40576
	s_nop 5
	v_cvt_pk_f16_f32 v0, v0, v1
	v_and_b32_e32 v1, 0x7fff7fff, v0
	v_cvt_pk_f16_f32 v2, v2, v3
	v_pk_fma_f16 v16, v1, s2, v164 op_sel_hi:[1,0,0]
	v_and_b32_e32 v3, 0x7fff7fff, v2
	v_pk_fma_f16 v16, v16, v1, s3 op_sel_hi:[1,1,0]
	v_pk_fma_f16 v18, v3, s2, v164 op_sel_hi:[1,0,0]
	v_pk_mul_f16 v16, v1, v16
	v_pk_fma_f16 v18, v18, v3, s3 op_sel_hi:[1,1,0]
	v_exp_f16_e32 v17, v16
	v_exp_f16_sdwa v16, v16 dst_sel:DWORD dst_unused:UNUSED_PAD src0_sel:WORD_1
	v_pk_mul_f16 v18, v3, v18
	v_pk_add_f16 v0, v1, v0
	v_exp_f16_e32 v19, v18
	v_exp_f16_sdwa v18, v18 dst_sel:DWORD dst_unused:UNUSED_PAD src0_sel:WORD_1
	v_pack_b32_f16 v16, v17, v16
	v_pk_fma_f16 v116, v1, v16, v0 neg_lo:[1,0,0] neg_hi:[1,0,0]
	v_pk_add_f16 v1, v3, v2
	v_pack_b32_f16 v0, v19, v18
	v_pk_fma_f16 v117, v3, v0, v1 neg_lo:[1,0,0] neg_hi:[1,0,0]
	v_cvt_pk_f16_f32 v0, v4, v5
	v_and_b32_e32 v1, 0x7fff7fff, v0
	v_pk_fma_f16 v2, v1, s2, v164 op_sel_hi:[1,0,0]
	s_waitcnt vmcnt(0) lgkmcnt(8)
	v_mfma_f32_32x32x16_f16 v[16:31], v[92:95], v[96:99], 0
	v_pk_fma_f16 v2, v2, v1, s3 op_sel_hi:[1,1,0]
	v_cvt_pk_f16_f32 v4, v6, v7
	v_pk_mul_f16 v2, v1, v2
	v_and_b32_e32 v5, 0x7fff7fff, v4
	v_exp_f16_e32 v3, v2
	v_exp_f16_sdwa v2, v2 dst_sel:DWORD dst_unused:UNUSED_PAD src0_sel:WORD_1
	v_pk_fma_f16 v6, v5, s2, v164 op_sel_hi:[1,0,0]
	v_pk_add_f16 v0, v1, v0
	v_pk_fma_f16 v6, v6, v5, s3 op_sel_hi:[1,1,0]
	v_pack_b32_f16 v2, v3, v2
	v_pk_mul_f16 v6, v5, v6
	v_pk_fma_f16 v118, v1, v2, v0 neg_lo:[1,0,0] neg_hi:[1,0,0]
	v_cvt_pk_f16_f32 v1, v8, v9
	v_exp_f16_e32 v7, v6
	v_exp_f16_sdwa v6, v6 dst_sel:DWORD dst_unused:UNUSED_PAD src0_sel:WORD_1
	v_and_b32_e32 v2, 0x7fff7fff, v1
	v_pk_fma_f16 v3, v2, s2, v164 op_sel_hi:[1,0,0]
	v_mfma_f32_32x32x16_f16 v[16:31], v[88:91], v[104:107], v[16:31]
	v_pk_fma_f16 v3, v3, v2, s3 op_sel_hi:[1,1,0]
	v_pack_b32_f16 v0, v7, v6
	v_pk_mul_f16 v3, v2, v3
	v_pk_add_f16 v4, v5, v4
	v_exp_f16_e32 v6, v3
	v_exp_f16_sdwa v3, v3 dst_sel:DWORD dst_unused:UNUSED_PAD src0_sel:WORD_1
	v_pk_fma_f16 v119, v5, v0, v4 neg_lo:[1,0,0] neg_hi:[1,0,0]
	v_cvt_pk_f16_f32 v4, v10, v11
	v_pk_add_f16 v1, v2, v1
	v_pack_b32_f16 v0, v6, v3
	v_and_b32_e32 v5, 0x7fff7fff, v4
	v_pk_fma_f16 v124, v2, v0, v1 neg_lo:[1,0,0] neg_hi:[1,0,0]
	v_pk_fma_f16 v0, v5, s2, v164 op_sel_hi:[1,0,0]
	v_mfma_f32_32x32x16_f16 v[16:31], v[84:87], v[100:103], v[16:31]
	v_pk_fma_f16 v0, v0, v5, s3 op_sel_hi:[1,1,0]
	v_addc_co_u32_e32 v137, vcc, 0, v157, vcc
	v_pk_mul_f16 v0, v5, v0
	ds_read_b128 v[84:87], v253 offset:43648
	v_exp_f16_e32 v6, v0
	v_exp_f16_sdwa v7, v0 dst_sel:DWORD dst_unused:UNUSED_PAD src0_sel:WORD_1
	ds_read_b128 v[0:3], v254 offset:3072
	s_waitcnt vmcnt(0) lgkmcnt(6)
	v_mfma_f32_32x32x16_f16 v[16:31], v[126:129], v[112:115], v[16:31]
	s_mov_b32 s6, 0xb000
	v_cvt_pk_f16_f32 v8, v12, v13
	v_and_b32_e32 v9, 0x7fff7fff, v8
	v_pk_fma_f16 v10, v9, s2, v164 op_sel_hi:[1,0,0]
	v_pack_b32_f16 v6, v6, v7
	v_pk_fma_f16 v10, v10, v9, s3 op_sel_hi:[1,1,0]
	v_pk_add_f16 v4, v5, v4
	v_mfma_f32_32x32x16_f16 v[16:31], v[144:147], v[108:111], v[16:31]
	v_pk_mul_f16 v10, v9, v10
	v_pk_fma_f16 v125, v5, v6, v4 neg_lo:[1,0,0] neg_hi:[1,0,0]
	v_exp_f16_e32 v11, v10
	v_exp_f16_sdwa v10, v10 dst_sel:DWORD dst_unused:UNUSED_PAD src0_sel:WORD_1
	v_pk_add_f16 v5, v9, v8
	v_pack_b32_f16 v4, v11, v10
	v_mfma_f32_32x32x16_f16 v[16:31], v[120:123], v[48:51], v[16:31]
	v_pk_fma_f16 v126, v9, v4, v5 neg_lo:[1,0,0] neg_hi:[1,0,0]
	v_cvt_pk_f16_f32 v4, v14, v15
	v_and_b32_e32 v5, 0x7fff7fff, v4
	v_pk_fma_f16 v6, v5, s2, v164 op_sel_hi:[1,0,0]
	v_pk_add_f16 v4, v5, v4
	v_pk_fma_f16 v6, v6, v5, s3 op_sel_hi:[1,1,0]
	v_mfma_f32_32x32x16_f16 v[16:31], v[148:151], v[52:55], v[16:31]
	v_add_co_u32_e32 v150, vcc, s7, v156
	v_pk_mul_f16 v6, v5, v6
	s_nop 0
	v_addc_co_u32_e32 v151, vcc, 0, v157, vcc
	ds_read_b128 v[88:91], v253 offset:45696
	v_add_co_u32_e32 v152, vcc, s6, v156
	v_mfma_f32_32x32x16_f16 v[16:31], v[36:39], v[56:59], v[16:31]
	s_nop 0
	v_addc_co_u32_e32 v153, vcc, 0, v157, vcc
	ds_read_b128 v[92:95], v253 offset:47744
	ds_read_b128 v[146:149], v253 offset:48768
	ds_read_b128 v[120:123], v253 offset:51840
	ds_read_b128 v[166:169], v253 offset:50816
	v_exp_f16_e32 v7, v6
	s_waitcnt vmcnt(0) lgkmcnt(10)
	v_mfma_f32_32x32x16_f16 v[16:31], v[64:67], v[60:63], v[16:31]
	ds_read_b128 v[64:67], v253 offset:49792
	v_exp_f16_sdwa v6, v6 dst_sel:DWORD dst_unused:UNUSED_PAD src0_sel:WORD_1
	s_mov_b32 s6, 0xe000
	v_add_co_u32_e32 v138, vcc, s6, v156
	v_pack_b32_f16 v6, v7, v6
	v_pk_fma_f16 v127, v5, v6, v4 neg_lo:[1,0,0] neg_hi:[1,0,0]
	s_nop 5
	v_cvt_pk_f16_f32 v8, v16, v17
	v_and_b32_e32 v9, 0x7fff7fff, v8
	v_pk_fma_f16 v10, v9, s2, v164 op_sel_hi:[1,0,0]
	v_pk_add_f16 v5, v9, v8
	v_pk_fma_f16 v10, v10, v9, s3 op_sel_hi:[1,1,0]
	v_addc_co_u32_e32 v139, vcc, 0, v157, vcc
	v_pk_mul_f16 v10, v9, v10
	v_cvt_pk_f16_f32 v8, v20, v21
	v_exp_f16_e32 v11, v10
	v_exp_f16_sdwa v10, v10 dst_sel:DWORD dst_unused:UNUSED_PAD src0_sel:WORD_1
	v_and_b32_e32 v20, 0x7fff7fff, v8
	v_pk_add_f16 v82, v20, v8
	ds_read_b128 v[36:39], v254 offset:2048
	v_pack_b32_f16 v4, v11, v10
	v_pk_fma_f16 v128, v9, v4, v5 neg_lo:[1,0,0] neg_hi:[1,0,0]
	v_cvt_pk_f16_f32 v4, v18, v19
	ds_read_b128 v[16:19], v254 offset:1024
	v_and_b32_e32 v5, 0x7fff7fff, v4
	v_pk_fma_f16 v6, v5, s2, v164 op_sel_hi:[1,0,0]
	v_pk_fma_f16 v9, v20, s2, v164 op_sel_hi:[1,0,0]
	v_pk_fma_f16 v6, v6, v5, s3 op_sel_hi:[1,1,0]
	v_pk_fma_f16 v9, v9, v20, s3 op_sel_hi:[1,1,0]
	v_pk_mul_f16 v6, v5, v6
	v_pk_mul_f16 v9, v20, v9
	v_exp_f16_e32 v7, v6
	v_exp_f16_sdwa v6, v6 dst_sel:DWORD dst_unused:UNUSED_PAD src0_sel:WORD_1
	v_exp_f16_e32 v10, v9
	v_exp_f16_sdwa v9, v9 dst_sel:DWORD dst_unused:UNUSED_PAD src0_sel:WORD_1
	v_pk_add_f16 v4, v5, v4
	v_pack_b32_f16 v6, v7, v6
	v_pk_fma_f16 v129, v5, v6, v4 neg_lo:[1,0,0] neg_hi:[1,0,0]
	v_pack_b32_f16 v21, v10, v9
	s_waitcnt vmcnt(0) lgkmcnt(8)
	v_mfma_f32_32x32x16_f16 v[0:15], v[0:3], v[96:99], 0
	v_pk_fma_f16 v130, v20, v21, v82 neg_lo:[1,0,0] neg_hi:[1,0,0]
	v_cvt_pk_f16_f32 v82, v22, v23
	v_and_b32_e32 v131, 0x7fff7fff, v82
	v_pk_fma_f16 v20, v131, s2, v164 op_sel_hi:[1,0,0]
	v_cvt_pk_f16_f32 v24, v24, v25
	v_pk_fma_f16 v20, v20, v131, s3 op_sel_hi:[1,1,0]
	v_and_b32_e32 v25, 0x7fff7fff, v24
	v_pk_mul_f16 v20, v131, v20
	v_mfma_f32_32x32x16_f16 v[0:15], v[132:135], v[104:107], v[0:15]
	v_exp_f16_e32 v144, v20
	v_exp_f16_sdwa v132, v20 dst_sel:DWORD dst_unused:UNUSED_PAD src0_sel:WORD_1
	v_pk_fma_f16 v20, v25, s2, v164 op_sel_hi:[1,0,0]
	ds_read_b128 v[152:155], v253 offset:46720
	v_pk_fma_f16 v20, v20, v25, s3 op_sel_hi:[1,1,0]
	v_pack_b32_f16 v132, v144, v132
	v_pk_mul_f16 v133, v25, v20
	ds_read_b128 v[20:23], v254 offset:4096
	v_mfma_f32_32x32x16_f16 v[0:15], v[140:143], v[100:103], v[0:15]
	ds_read_b128 v[142:145], v253 offset:42624
	v_cvt_pk_f16_f32 v26, v26, v27
	v_and_b32_e32 v27, 0x7fff7fff, v26
	v_exp_f16_e32 v134, v133
	v_exp_f16_sdwa v133, v133 dst_sel:DWORD dst_unused:UNUSED_PAD src0_sel:WORD_1
	v_pk_add_f16 v82, v131, v82
	v_pk_add_f16 v24, v25, v24
	v_mfma_f32_32x32x16_f16 v[0:15], v[84:87], v[112:115], v[0:15]
	v_pk_fma_f16 v84, v27, s2, v164 op_sel_hi:[1,0,0]
	v_pk_fma_f16 v131, v131, v132, v82 neg_lo:[1,0,0] neg_hi:[1,0,0]
	v_pk_fma_f16 v84, v84, v27, s3 op_sel_hi:[1,1,0]
	v_pack_b32_f16 v82, v134, v133
	v_pk_mul_f16 v84, v27, v84
	v_pk_fma_f16 v132, v25, v82, v24 neg_lo:[1,0,0] neg_hi:[1,0,0]
	v_exp_f16_e32 v85, v84
	s_waitcnt vmcnt(0) lgkmcnt(10)
	v_mfma_f32_32x32x16_f16 v[0:15], v[88:91], v[108:111], v[0:15]
	v_exp_f16_sdwa v84, v84 dst_sel:DWORD dst_unused:UNUSED_PAD src0_sel:WORD_1
	v_pk_add_f16 v25, v27, v26
	ds_read_b128 v[170:173], v254
	s_mov_b32 s6, 0x13000
	v_pack_b32_f16 v24, v85, v84
	v_pk_fma_f16 v133, v27, v24, v25 neg_lo:[1,0,0] neg_hi:[1,0,0]
	v_cvt_pk_f16_f32 v24, v28, v29
	s_waitcnt vmcnt(0) lgkmcnt(10)
	v_mfma_f32_32x32x16_f16 v[0:15], v[92:95], v[72:75], v[0:15]
	v_and_b32_e32 v25, 0x7fff7fff, v24
	v_cvt_pk_f16_f32 v28, v30, v31
	v_pk_fma_f16 v26, v25, s2, v164 op_sel_hi:[1,0,0]
	v_and_b32_e32 v29, 0x7fff7fff, v28
	v_pk_fma_f16 v26, v26, v25, s3 op_sel_hi:[1,1,0]
	v_pk_fma_f16 v30, v29, s2, v164 op_sel_hi:[1,0,0]
	v_pk_mul_f16 v26, v25, v26
	s_waitcnt vmcnt(0) lgkmcnt(6)
	v_mfma_f32_32x32x16_f16 v[0:15], v[64:67], v[68:71], v[0:15]
	v_pk_fma_f16 v30, v30, v29, s3 op_sel_hi:[1,1,0]
	v_exp_f16_e32 v27, v26
	v_exp_f16_sdwa v26, v26 dst_sel:DWORD dst_unused:UNUSED_PAD src0_sel:WORD_1
	v_pk_mul_f16 v30, v29, v30
	v_pk_add_f16 v24, v25, v24
	v_exp_f16_e32 v31, v30
	v_exp_f16_sdwa v30, v30 dst_sel:DWORD dst_unused:UNUSED_PAD src0_sel:WORD_1
	v_mfma_f32_32x32x16_f16 v[0:15], v[120:123], v[40:43], v[0:15]
	v_pack_b32_f16 v26, v27, v26
	v_pk_fma_f16 v134, v25, v26, v24 neg_lo:[1,0,0] neg_hi:[1,0,0]
	v_pack_b32_f16 v24, v31, v30
	v_pk_add_f16 v25, v29, v28
	v_add_co_u32_e32 v150, vcc, s6, v156
	v_pk_fma_f16 v135, v29, v24, v25 neg_lo:[1,0,0] neg_hi:[1,0,0]
	s_waitcnt vmcnt(0) lgkmcnt(4)
	v_mfma_f32_32x32x16_f16 v[0:15], v[16:19], v[32:35], v[0:15]
	v_addc_co_u32_e32 v151, vcc, 0, v157, vcc
	ds_read_b128 v[64:67], v254 offset:5120
	ds_read_b128 v[84:87], v254 offset:7168
	s_mov_b32 s6, 0x10000
	v_add_co_u32_e32 v140, vcc, s6, v156
	s_nop 6
	v_cvt_pk_f16_f32 v16, v0, v1
	v_and_b32_e32 v17, 0x7fff7fff, v16
	v_pk_fma_f16 v0, v17, s2, v164 op_sel_hi:[1,0,0]
	v_cvt_pk_f16_f32 v24, v2, v3
	v_pk_fma_f16 v0, v0, v17, s3 op_sel_hi:[1,1,0]
	v_and_b32_e32 v25, 0x7fff7fff, v24
	v_pk_mul_f16 v0, v17, v0
	v_pk_add_f16 v16, v17, v16
	v_exp_f16_e32 v18, v0
	v_exp_f16_sdwa v19, v0 dst_sel:DWORD dst_unused:UNUSED_PAD src0_sel:WORD_1
	v_pk_fma_f16 v0, v25, s2, v164 op_sel_hi:[1,0,0]
	v_addc_co_u32_e32 v141, vcc, 0, v157, vcc
	v_pk_fma_f16 v0, v0, v25, s3 op_sel_hi:[1,1,0]
	v_pack_b32_f16 v18, v18, v19
	v_pk_mul_f16 v26, v25, v0
	ds_read_b128 v[0:3], v254 offset:21824
	v_exp_f16_e32 v27, v26
	v_exp_f16_sdwa v26, v26 dst_sel:DWORD dst_unused:UNUSED_PAD src0_sel:WORD_1
	v_pk_fma_f16 v120, v17, v18, v16 neg_lo:[1,0,0] neg_hi:[1,0,0]
	v_pk_add_f16 v17, v25, v24
	ds_read_b128 v[88:91], v254 offset:9216
	v_pack_b32_f16 v16, v27, v26
	v_pk_fma_f16 v121, v25, v16, v17 neg_lo:[1,0,0] neg_hi:[1,0,0]
	s_waitcnt vmcnt(0) lgkmcnt(6)
	v_mfma_f32_32x32x16_f16 v[16:31], v[20:23], v[96:99], 0
	v_cvt_pk_f16_f32 v82, v4, v5
	s_mov_b32 s6, 0xf000
	v_and_b32_e32 v122, 0x7fff7fff, v82
	v_add_co_u32_e32 v162, vcc, s6, v156
	v_pk_fma_f16 v4, v122, s2, v164 op_sel_hi:[1,0,0]
	s_nop 0
	v_addc_co_u32_e32 v163, vcc, 0, v157, vcc
	v_mfma_f32_32x32x16_f16 v[16:31], v[44:47], v[104:107], v[16:31]
	v_pk_fma_f16 v4, v4, v122, s3 op_sel_hi:[1,1,0]
	ds_read_b128 v[92:95], v254 offset:11264
	v_pk_mul_f16 v4, v122, v4
	v_cvt_pk_f16_f32 v45, v6, v7
	v_exp_f16_e32 v5, v4
	v_exp_f16_sdwa v4, v4 dst_sel:DWORD dst_unused:UNUSED_PAD src0_sel:WORD_1
	v_and_b32_e32 v46, 0x7fff7fff, v45
	s_waitcnt vmcnt(0) lgkmcnt(6)
	v_mfma_f32_32x32x16_f16 v[16:31], v[142:145], v[100:103], v[16:31]
	s_mov_b32 s6, 0x11000
	v_pack_b32_f16 v44, v5, v4
	v_pk_fma_f16 v4, v46, s2, v164 op_sel_hi:[1,0,0]
	v_cvt_pk_f16_f32 v10, v10, v11
	v_pk_fma_f16 v4, v4, v46, s3 op_sel_hi:[1,1,0]
	v_and_b32_e32 v11, 0x7fff7fff, v10
	v_pk_mul_f16 v47, v46, v4
	v_mfma_f32_32x32x16_f16 v[16:31], v[76:79], v[112:115], v[16:31]
	ds_read_b128 v[4:7], v254 offset:13312
	v_exp_f16_e32 v76, v47
	v_exp_f16_sdwa v47, v47 dst_sel:DWORD dst_unused:UNUSED_PAD src0_sel:WORD_1
	v_pk_add_f16 v77, v122, v82
	v_pk_add_f16 v45, v46, v45
	v_pk_fma_f16 v122, v122, v44, v77 neg_lo:[1,0,0] neg_hi:[1,0,0]
	v_pack_b32_f16 v44, v76, v47
	v_mfma_f32_32x32x16_f16 v[16:31], v[152:155], v[108:111], v[16:31]
	ds_read_b128 v[76:79], v254 offset:15360
	v_cvt_pk_f16_f32 v47, v8, v9
	v_add_co_u32_e32 v8, vcc, s6, v156
	v_and_b32_e32 v82, 0x7fff7fff, v47
	s_nop 0
	v_addc_co_u32_e32 v9, vcc, 0, v157, vcc
	v_mfma_f32_32x32x16_f16 v[16:31], v[146:149], v[72:75], v[16:31]
	ds_read_b128 v[72:75], v254 offset:17728
	v_pk_fma_f16 v123, v82, s2, v164 op_sel_hi:[1,0,0]
	s_mov_b32 s6, 0x12000
	v_pk_fma_f16 v123, v123, v82, s3 op_sel_hi:[1,1,0]
	v_add_co_u32_e32 v160, vcc, s6, v156
	ds_read_b128 v[146:149], v254 offset:6144
	v_mfma_f32_32x32x16_f16 v[16:31], v[166:169], v[68:71], v[16:31]
	v_pk_mul_f16 v68, v82, v123
	v_addc_co_u32_e32 v161, vcc, 0, v157, vcc
	v_exp_f16_e32 v136, v68
	v_exp_f16_sdwa v137, v68 dst_sel:DWORD dst_unused:UNUSED_PAD src0_sel:WORD_1
	ds_read_b128 v[68:71], v254 offset:19776
	ds_read_b128 v[142:145], v254 offset:22848
	s_waitcnt vmcnt(0) lgkmcnt(11)
	v_mfma_f32_32x32x16_f16 v[16:31], v[170:173], v[40:43], v[16:31]
	v_pk_fma_f16 v123, v46, v44, v45 neg_lo:[1,0,0] neg_hi:[1,0,0]
	v_pack_b32_f16 v136, v136, v137
	v_pk_add_f16 v137, v82, v47
	ds_read_b128 v[170:173], v254 offset:16384
	v_pk_fma_f16 v136, v82, v136, v137 neg_lo:[1,0,0] neg_hi:[1,0,0]
	s_mov_b32 s6, 0x16000
	ds_read_b128 v[152:155], v254 offset:25920
	v_mfma_f32_32x32x16_f16 v[16:31], v[36:39], v[32:35], v[16:31]
	v_pk_fma_f16 v32, v11, s2, v164 op_sel_hi:[1,0,0]
	s_nop 0
	v_pk_fma_f16 v32, v32, v11, s3 op_sel_hi:[1,1,0]
	s_nop 0
	v_pk_mul_f16 v32, v11, v32
	s_nop 6
	v_cvt_pk_f16_f32 v24, v24, v25
	v_exp_f16_e32 v165, v32
	v_exp_f16_sdwa v166, v32 dst_sel:DWORD dst_unused:UNUSED_PAD src0_sel:WORD_1
	s_waitcnt vmcnt(0) lgkmcnt(10)
	v_mfma_f32_32x32x16_f16 v[32:47], v[0:3], v[96:99], 0
	v_pk_add_f16 v1, v11, v10
	v_cvt_pk_f16_f32 v10, v14, v15
	v_pack_b32_f16 v0, v165, v166
	ds_read_b128 v[166:169], v254 offset:8192
	v_pk_fma_f16 v137, v11, v0, v1 neg_lo:[1,0,0] neg_hi:[1,0,0]
	v_cvt_pk_f16_f32 v0, v12, v13
	v_and_b32_e32 v1, 0x7fff7fff, v0
	v_mfma_f32_32x32x16_f16 v[32:47], v[64:67], v[104:107], v[32:47]
	ds_read_b128 v[64:67], v254 offset:10240
	v_pk_fma_f16 v2, v1, s2, v164 op_sel_hi:[1,0,0]
	v_and_b32_e32 v11, 0x7fff7fff, v10
	v_pk_fma_f16 v2, v2, v1, s3 op_sel_hi:[1,1,0]
	v_pk_fma_f16 v12, v11, s2, v164 op_sel_hi:[1,0,0]
	v_pk_mul_f16 v2, v1, v2
	v_pk_fma_f16 v12, v12, v11, s3 op_sel_hi:[1,1,0]
	v_mfma_f32_32x32x16_f16 v[32:47], v[84:87], v[100:103], v[32:47]
	v_exp_f16_e32 v3, v2
	v_exp_f16_sdwa v2, v2 dst_sel:DWORD dst_unused:UNUSED_PAD src0_sel:WORD_1
	v_pk_mul_f16 v12, v11, v12
	v_pk_add_f16 v0, v1, v0
	v_exp_f16_e32 v13, v12
	v_exp_f16_sdwa v12, v12 dst_sel:DWORD dst_unused:UNUSED_PAD src0_sel:WORD_1
	v_pack_b32_f16 v2, v3, v2
	s_waitcnt vmcnt(0) lgkmcnt(11)
	v_mfma_f32_32x32x16_f16 v[32:47], v[88:91], v[112:115], v[32:47]
	ds_read_b128 v[88:91], v254 offset:12288
	v_pk_fma_f16 v138, v1, v2, v0 neg_lo:[1,0,0] neg_hi:[1,0,0]
	v_pack_b32_f16 v0, v13, v12
	v_pk_add_f16 v1, v11, v10
	v_add_co_u32_e32 v162, vcc, s6, v156
	v_pk_fma_f16 v139, v11, v0, v1 neg_lo:[1,0,0] neg_hi:[1,0,0]
	s_waitcnt vmcnt(0) lgkmcnt(11)
	v_mfma_f32_32x32x16_f16 v[32:47], v[92:95], v[108:111], v[32:47]
	ds_read_b128 v[92:95], v254 offset:14336
	v_cvt_pk_f16_f32 v0, v16, v17
	v_and_b32_e32 v1, 0x7fff7fff, v0
	v_pk_fma_f16 v2, v1, s2, v164 op_sel_hi:[1,0,0]
	v_pk_add_f16 v0, v1, v0
	v_pk_fma_f16 v2, v2, v1, s3 op_sel_hi:[1,1,0]
	v_addc_co_u32_e32 v163, vcc, 0, v157, vcc
	s_waitcnt vmcnt(0) lgkmcnt(11)
	v_mfma_f32_32x32x16_f16 v[32:47], v[4:7], v[48:51], v[32:47]
	v_cvt_pk_f16_f32 v4, v18, v19
	v_and_b32_e32 v5, 0x7fff7fff, v4
	ds_read_b128 v[16:19], v254 offset:18752
	v_pk_fma_f16 v6, v5, s2, v164 op_sel_hi:[1,0,0]
	v_pk_mul_f16 v2, v1, v2
	v_pk_fma_f16 v6, v6, v5, s3 op_sel_hi:[1,1,0]
	v_exp_f16_e32 v3, v2
	s_waitcnt vmcnt(0) lgkmcnt(11)
	v_mfma_f32_32x32x16_f16 v[32:47], v[76:79], v[52:55], v[32:47]
	v_exp_f16_sdwa v2, v2 dst_sel:DWORD dst_unused:UNUSED_PAD src0_sel:WORD_1
	v_pk_mul_f16 v6, v5, v6
	ds_read_b128 v[84:87], v254 offset:28992
	v_exp_f16_e32 v7, v6
	v_exp_f16_sdwa v6, v6 dst_sel:DWORD dst_unused:UNUSED_PAD src0_sel:WORD_1
	v_pack_b32_f16 v2, v3, v2
	v_pk_fma_f16 v140, v1, v2, v0 neg_lo:[1,0,0] neg_hi:[1,0,0]
	s_waitcnt vmcnt(0) lgkmcnt(11)
	v_mfma_f32_32x32x16_f16 v[32:47], v[72:75], v[56:59], v[32:47]
	v_pack_b32_f16 v0, v7, v6
	ds_read_b128 v[72:75], v254 offset:20800
	v_pk_add_f16 v1, v5, v4
	s_mov_b32 s6, 0x14000
	v_pk_fma_f16 v141, v5, v0, v1 neg_lo:[1,0,0] neg_hi:[1,0,0]
	v_lshlrev_b32_e32 v0, 2, v159
	v_ashrrev_i32_e32 v1, 31, v0
	v_lshl_add_u64 v[0:1], v[0:1], 2, v[80:81]
	global_load_dwordx4 v[76:79], v[0:1], off
	s_waitcnt vmcnt(1) lgkmcnt(10)
	v_mfma_f32_32x32x16_f16 v[32:47], v[68:71], v[60:63], v[32:47]
	ds_read_b128 v[68:71], v254 offset:40576
	ds_read_b128 v[174:177], v254 offset:23872
	s_waitcnt vmcnt(0) lgkmcnt(2)
	v_cvt_pk_f16_f32 v79, v20, v21
	v_and_b32_e32 v80, 0x7fff7fff, v79
	v_pk_fma_f16 v20, v80, s2, v164 op_sel_hi:[1,0,0]
	v_pk_add_f16 v79, v80, v79
	v_pk_fma_f16 v20, v20, v80, s3 op_sel_hi:[1,1,0]
	v_and_b32_e32 v25, 0x7fff7fff, v24
	v_mfma_f32_32x32x16_f16 v[0:15], v[142:145], v[96:99], 0
	v_cvt_pk_f16_f32 v143, v22, v23
	v_pk_mul_f16 v20, v80, v20
	v_and_b32_e32 v144, 0x7fff7fff, v143
	v_exp_f16_e32 v81, v20
	v_exp_f16_sdwa v82, v20 dst_sel:DWORD dst_unused:UNUSED_PAD src0_sel:WORD_1
	v_pk_fma_f16 v20, v144, s2, v164 op_sel_hi:[1,0,0]
	v_cvt_pk_f16_f32 v26, v26, v27
	v_pk_fma_f16 v20, v20, v144, s3 op_sel_hi:[1,1,0]
	v_mfma_f32_32x32x16_f16 v[0:15], v[146:149], v[104:107], v[0:15]
	v_pk_mul_f16 v142, v144, v20
	ds_read_b128 v[20:23], v254 offset:27968
	v_add_co_u32_e32 v148, vcc, s6, v156
	s_mov_b32 s6, 0x15000
	s_nop 0
	v_addc_co_u32_e32 v149, vcc, 0, v157, vcc
	v_mfma_f32_32x32x16_f16 v[0:15], v[166:169], v[100:103], v[0:15]
	ds_read_b128 v[166:169], v254 offset:32064
	ds_read_b128 v[178:181], v254 offset:24896
	v_add_co_u32_e32 v194, vcc, s6, v156
	v_exp_f16_e32 v145, v142
	s_nop 0
	v_addc_co_u32_e32 v195, vcc, 0, v157, vcc
	v_exp_f16_sdwa v146, v142 dst_sel:DWORD dst_unused:UNUSED_PAD src0_sel:WORD_1
	v_mfma_f32_32x32x16_f16 v[0:15], v[64:67], v[112:115], v[0:15]
	ds_read_b128 v[64:67], v254 offset:36480
	v_pack_b32_f16 v81, v81, v82
	v_pk_fma_f16 v142, v80, v81, v79 neg_lo:[1,0,0] neg_hi:[1,0,0]
	v_pack_b32_f16 v79, v145, v146
	v_pk_add_f16 v80, v144, v143
	s_mov_b32 s6, 0x18000
	v_pk_fma_f16 v143, v144, v79, v80 neg_lo:[1,0,0] neg_hi:[1,0,0]
	v_mfma_f32_32x32x16_f16 v[0:15], v[88:91], v[108:111], v[0:15]
	ds_read_b128 v[88:91], v254 offset:41600
	v_pk_fma_f16 v79, v25, s2, v164 op_sel_hi:[1,0,0]
	v_add_co_u32_e32 v160, vcc, s6, v156
	v_pk_fma_f16 v79, v79, v25, s3 op_sel_hi:[1,1,0]
	v_pk_add_f16 v24, v25, v24
	v_pk_mul_f16 v79, v25, v79
	v_mfma_f32_32x32x16_f16 v[0:15], v[92:95], v[48:51], v[0:15]
	ds_read_b128 v[92:95], v254 offset:33088
	ds_read_b128 v[186:189], v254 offset:31040
	v_exp_f16_e32 v48, v79
	v_exp_f16_sdwa v49, v79 dst_sel:DWORD dst_unused:UNUSED_PAD src0_sel:WORD_1
	v_addc_co_u32_e32 v161, vcc, 0, v157, vcc
	v_and_b32_e32 v27, 0x7fff7fff, v26
	v_mfma_f32_32x32x16_f16 v[0:15], v[170:173], v[52:55], v[0:15]
	v_pack_b32_f16 v48, v48, v49
	v_pk_fma_f16 v144, v25, v48, v24 neg_lo:[1,0,0] neg_hi:[1,0,0]
	v_cvt_pk_f16_f32 v25, v28, v29
	v_pk_fma_f16 v50, v27, s2, v164 op_sel_hi:[1,0,0]
	v_mov_b32_e32 v82, v83
	v_pk_fma_f16 v50, v50, v27, s3 op_sel_hi:[1,1,0]
	ds_read_b128 v[170:173], v254 offset:30016
	v_mfma_f32_32x32x16_f16 v[0:15], v[16:19], v[56:59], v[0:15]
	v_pk_mul_f16 v50, v27, v50
	ds_read_b128 v[182:185], v254 offset:34112
	v_exp_f16_e32 v51, v50
	v_exp_f16_sdwa v50, v50 dst_sel:DWORD dst_unused:UNUSED_PAD src0_sel:WORD_1
	v_and_b32_e32 v16, 0x7fff7fff, v25
	v_pk_fma_f16 v17, v16, s2, v164 op_sel_hi:[1,0,0]
	s_mov_b32 s6, 0x17000
	v_mfma_f32_32x32x16_f16 v[0:15], v[72:75], v[60:63], v[0:15]
	ds_read_b128 v[72:75], v254 offset:37504
	v_pack_b32_f16 v24, v51, v50
	v_cvt_pk_f16_f32 v19, v76, v77
	v_cvt_pk_f16_f32 v28, v78, 1.0
	ds_read_b128 v[76:79], v254 offset:42624
	v_cndmask_b32_e64 v80, 0, v19, s[4:5]
	v_cndmask_b32_e64 v81, 0, v28, s[4:5]
	v_pk_fma_f16 v17, v17, v16, s3 op_sel_hi:[1,1,0]
	v_add_co_u32_e32 v202, vcc, s6, v156
	s_waitcnt vmcnt(0) lgkmcnt(12)
	v_mfma_f32_32x32x16_f16 v[48:63], v[68:71], v[80:83], 0
	v_pk_mul_f16 v17, v16, v17
	v_addc_co_u32_e32 v203, vcc, 0, v157, vcc
	v_exp_f16_e32 v18, v17
	v_exp_f16_sdwa v17, v17 dst_sel:DWORD dst_unused:UNUSED_PAD src0_sel:WORD_1
	ds_read_b128 v[190:193], v254 offset:43648
	v_pk_add_f16 v19, v27, v26
	s_waitcnt vmcnt(0) lgkmcnt(12)
	v_mfma_f32_32x32x16_f16 v[48:63], v[174:177], v[116:119], v[48:63]
	v_pk_fma_f16 v145, v27, v24, v19 neg_lo:[1,0,0] neg_hi:[1,0,0]
	v_pack_b32_f16 v17, v18, v17
	v_pk_add_f16 v18, v16, v25
	v_cvt_pk_f16_f32 v19, v30, v31
	v_and_b32_e32 v24, 0x7fff7fff, v19
	v_pk_fma_f16 v146, v16, v17, v18 neg_lo:[1,0,0] neg_hi:[1,0,0]
	v_cvt_pk_f16_f32 v17, v32, v33
	s_waitcnt vmcnt(0) lgkmcnt(11)
	v_mfma_f32_32x32x16_f16 v[48:63], v[20:23], v[124:127], v[48:63]
	v_pk_fma_f16 v25, v24, s2, v164 op_sel_hi:[1,0,0]
	v_and_b32_e32 v32, 0x7fff7fff, v17
	v_pk_fma_f16 v25, v25, v24, s3 op_sel_hi:[1,1,0]
	v_pk_fma_f16 v18, v32, s2, v164 op_sel_hi:[1,0,0]
	v_pk_mul_f16 v25, v24, v25
	v_pk_fma_f16 v18, v18, v32, s3 op_sel_hi:[1,1,0]
	v_exp_f16_e32 v26, v25
	s_waitcnt vmcnt(0) lgkmcnt(10)
	v_mfma_f32_32x32x16_f16 v[48:63], v[166:169], v[128:131], v[48:63]
	ds_read_b128 v[166:169], v254 offset:38528
	v_exp_f16_sdwa v25, v25 dst_sel:DWORD dst_unused:UNUSED_PAD src0_sel:WORD_1
	ds_read_b128 v[174:177], v254 offset:26944
	v_pk_mul_f16 v18, v32, v18
	v_pk_add_f16 v19, v24, v19
	v_exp_f16_e32 v20, v18
	v_exp_f16_sdwa v18, v18 dst_sel:DWORD dst_unused:UNUSED_PAD src0_sel:WORD_1
	v_pack_b32_f16 v16, v26, v25
	v_pk_fma_f16 v147, v24, v16, v19 neg_lo:[1,0,0] neg_hi:[1,0,0]
	s_waitcnt vmcnt(0) lgkmcnt(10)
	v_mfma_f32_32x32x16_f16 v[48:63], v[64:67], v[132:135], v[48:63]
	v_pack_b32_f16 v33, v20, v18
	v_pk_add_f16 v64, v32, v17
	v_cvt_pk_f16_f32 v36, v36, v37
	v_pk_fma_f16 v148, v32, v33, v64 neg_lo:[1,0,0] neg_hi:[1,0,0]
	v_cvt_pk_f16_f32 v32, v34, v35
	v_and_b32_e32 v33, 0x7fff7fff, v32
	v_pk_fma_f16 v34, v33, s2, v164 op_sel_hi:[1,0,0]
	s_waitcnt vmcnt(0) lgkmcnt(9)
	v_mfma_f32_32x32x16_f16 v[16:31], v[88:91], v[80:83], 0
	v_pk_fma_f16 v34, v34, v33, s3 op_sel_hi:[1,1,0]
	v_and_b32_e32 v37, 0x7fff7fff, v36
	v_pk_mul_f16 v34, v33, v34
	v_pk_add_f16 v32, v33, v32
	v_exp_f16_e32 v35, v34
	v_exp_f16_sdwa v34, v34 dst_sel:DWORD dst_unused:UNUSED_PAD src0_sel:WORD_1
	v_pk_fma_f16 v64, v37, s2, v164 op_sel_hi:[1,0,0]
	v_mfma_f32_32x32x16_f16 v[16:31], v[178:181], v[116:119], v[16:31]
	v_pk_fma_f16 v64, v64, v37, s3 op_sel_hi:[1,1,0]
	v_pack_b32_f16 v34, v35, v34
	v_pk_fma_f16 v149, v33, v34, v32 neg_lo:[1,0,0] neg_hi:[1,0,0]
	ds_read_b128 v[32:35], v254 offset:35456
	v_pk_mul_f16 v64, v37, v64
	v_pk_add_f16 v36, v37, v36
	v_exp_f16_e32 v65, v64
	v_exp_f16_sdwa v64, v64 dst_sel:DWORD dst_unused:UNUSED_PAD src0_sel:WORD_1
	v_mfma_f32_32x32x16_f16 v[16:31], v[84:87], v[124:127], v[16:31]
	v_cvt_pk_f16_f32 v84, v38, v39
	v_and_b32_e32 v85, 0x7fff7fff, v84
	v_pack_b32_f16 v64, v65, v64
	v_pk_fma_f16 v150, v37, v64, v36 neg_lo:[1,0,0] neg_hi:[1,0,0]
	v_pk_fma_f16 v36, v85, s2, v164 op_sel_hi:[1,0,0]
	s_mov_b32 s6, 0x1b000
	v_pk_fma_f16 v64, v36, v85, s3 op_sel_hi:[1,1,0]
	ds_read_b128 v[36:39], v254 offset:39552
	s_waitcnt vmcnt(0) lgkmcnt(10)
	v_mfma_f32_32x32x16_f16 v[16:31], v[92:95], v[128:131], v[16:31]
	v_add_co_u32_e32 v204, vcc, s6, v156
	v_pk_mul_f16 v86, v85, v64
	s_nop 0
	v_addc_co_u32_e32 v205, vcc, 0, v157, vcc
	ds_read_b128 v[178:181], v255 offset:8192
	ds_read_b128 v[194:197], v254 offset:46720
	ds_read_b128 v[198:201], v254 offset:44672
	s_waitcnt vmcnt(0) lgkmcnt(9)
	v_mfma_f32_32x32x16_f16 v[16:31], v[72:75], v[132:135], v[16:31]
	v_cvt_pk_f16_f32 v40, v40, v41
	v_and_b32_e32 v41, 0x7fff7fff, v40
	v_pk_fma_f16 v88, v41, s2, v164 op_sel_hi:[1,0,0]
	v_exp_f16_e32 v87, v86
	v_pk_fma_f16 v88, v88, v41, s3 op_sel_hi:[1,1,0]
	v_exp_f16_sdwa v86, v86 dst_sel:DWORD dst_unused:UNUSED_PAD src0_sel:WORD_1
	v_pk_mul_f16 v88, v41, v88
	s_waitcnt vmcnt(0) lgkmcnt(8)
	v_mfma_f32_32x32x16_f16 v[64:79], v[76:79], v[80:83], 0
	v_exp_f16_e32 v89, v88
	v_exp_f16_sdwa v88, v88 dst_sel:DWORD dst_unused:UNUSED_PAD src0_sel:WORD_1
	v_pack_b32_f16 v86, v87, v86
	v_pk_add_f16 v84, v85, v84
	v_pk_add_f16 v40, v41, v40
	v_pk_fma_f16 v151, v85, v86, v84 neg_lo:[1,0,0] neg_hi:[1,0,0]
	v_pack_b32_f16 v84, v89, v88
	v_mfma_f32_32x32x16_f16 v[64:79], v[152:155], v[116:119], v[64:79]
	v_pk_fma_f16 v152, v41, v84, v40 neg_lo:[1,0,0] neg_hi:[1,0,0]
	v_cvt_pk_f16_f32 v153, v42, v43
	ds_read_b128 v[40:43], v254 offset:48768
	s_mov_b32 s6, 0x1a000
	v_add_co_u32_e32 v154, vcc, s6, v156
	s_mov_b32 s6, 0x19000
	v_mfma_f32_32x32x16_f16 v[64:79], v[170:173], v[124:127], v[64:79]
	v_addc_co_u32_e32 v155, vcc, 0, v157, vcc
	ds_read_b128 v[170:173], v254 offset:50816
	v_add_co_u32_e32 v162, vcc, s6, v156
	v_and_b32_e32 v159, 0x7fff7fff, v153
	s_nop 0
	v_addc_co_u32_e32 v163, vcc, 0, v157, vcc
	v_mfma_f32_32x32x16_f16 v[64:79], v[182:185], v[128:131], v[64:79]
	v_pk_fma_f16 v84, v159, s2, v164 op_sel_hi:[1,0,0]
	ds_read_b128 v[182:185], v255 offset:2048
	v_pk_fma_f16 v84, v84, v159, s3 op_sel_hi:[1,1,0]
	s_mov_b32 s6, 0x1c000
	v_pk_mul_f16 v84, v159, v84
	v_cvt_pk_f16_f32 v48, v48, v49
	v_exp_f16_e32 v165, v84
	s_waitcnt vmcnt(0) lgkmcnt(9)
	v_mfma_f32_32x32x16_f16 v[64:79], v[166:169], v[132:135], v[64:79]
	ds_read_b128 v[166:169], v255
	v_exp_f16_sdwa v206, v84 dst_sel:DWORD dst_unused:UNUSED_PAD src0_sel:WORD_1
	v_cvt_pk_f16_f32 v49, v50, v51
	v_cvt_pk_f16_f32 v50, v52, v53
	v_cvt_pk_f16_f32 v51, v54, v55
	v_cvt_pk_f16_f32 v24, v24, v25
	v_cvt_pk_f16_f32 v25, v26, v27
	v_mfma_f32_32x32x16_f16 v[80:95], v[190:193], v[80:83], 0
	v_cvt_pk_f16_f32 v26, v28, v29
	v_cvt_pk_f16_f32 v27, v30, v31
	ds_read_b128 v[28:31], v254 offset:49792
	v_cvt_pk_f16_f32 v20, v20, v21
	v_cvt_pk_f16_f32 v21, v22, v23
	v_pk_max_f16 v23, v21, 0
	v_pk_max_f16 v22, v20, 0
	s_waitcnt vmcnt(0) lgkmcnt(10)
	v_mfma_f32_32x32x16_f16 v[80:95], v[174:177], v[116:119], v[80:95]
	ds_read_b128 v[116:119], v255 offset:4096
	v_pk_max_f16 v176, v50, 0
	v_pk_max_f16 v175, v49, 0
	v_pk_max_f16 v174, v48, 0
	v_cvt_pk_f16_f32 v48, v56, v57
	v_cvt_pk_f16_f32 v49, v58, v59
	v_cvt_pk_f16_f32 v50, v60, v61
	v_mfma_f32_32x32x16_f16 v[80:95], v[186:189], v[124:127], v[80:95]
	v_add_co_u32_e32 v186, vcc, s6, v156
	v_pk_max_f16 v177, v51, 0
	s_nop 0
	v_addc_co_u32_e32 v187, vcc, 0, v157, vcc
	ds_read_b128 v[124:127], v255 offset:6144
	v_pk_max_f16 v27, v27, 0
	s_waitcnt vmcnt(0) lgkmcnt(11)
	v_mfma_f32_32x32x16_f16 v[80:95], v[32:35], v[128:131], v[80:95]
	v_cvt_pk_f16_f32 v32, v62, v63
	v_pk_max_f16 v131, v32, 0
	ds_read_b128 v[32:35], v255 offset:9216
	v_pk_max_f16 v130, v50, 0
	v_pk_max_f16 v129, v49, 0
	v_pk_max_f16 v128, v48, 0
	v_pk_max_f16 v26, v26, 0
	s_waitcnt vmcnt(0) lgkmcnt(11)
	v_mfma_f32_32x32x16_f16 v[80:95], v[36:39], v[132:135], v[80:95]
	v_cvt_pk_f16_f32 v36, v16, v17
	v_cvt_pk_f16_f32 v37, v18, v19
	ds_read_b128 v[16:19], v254 offset:45696
	ds_read_b128 v[132:135], v254 offset:47744
	v_cvt_pk_f16_f32 v38, v68, v69
	v_cvt_pk_f16_f32 v39, v70, v71
	ds_read_b128 v[68:71], v254 offset:51840
	s_waitcnt vmcnt(0) lgkmcnt(13)
	v_mfma_f32_32x32x16_f16 v[48:63], v[178:181], v[96:99], 0
	v_pk_max_f16 v21, v37, 0
	v_pk_max_f16 v20, v36, 0
	v_cvt_pk_f16_f32 v36, v64, v65
	v_cvt_pk_f16_f32 v37, v66, v67
	v_pk_max_f16 v65, v37, 0
	v_pk_max_f16 v64, v36, 0
	v_cvt_pk_f16_f32 v36, v72, v73
	s_waitcnt vmcnt(0) lgkmcnt(11)
	v_mfma_f32_32x32x16_f16 v[48:63], v[198:201], v[174:177], v[48:63]
	v_cvt_pk_f16_f32 v37, v74, v75
	ds_read_b128 v[72:75], v255 offset:1024
	v_pk_max_f16 v25, v25, 0
	v_pk_max_f16 v24, v24, 0
	v_pk_max_f16 v67, v39, 0
	v_pk_max_f16 v66, v38, 0
	ds_read_b128 v[160:163], v255 offset:3072
	v_mfma_f32_32x32x16_f16 v[48:63], v[194:197], v[128:131], v[48:63]
	v_cvt_pk_f16_f32 v38, v76, v77
	v_cvt_pk_f16_f32 v39, v78, v79
	v_pk_max_f16 v79, v39, 0
	v_pk_max_f16 v78, v38, 0
	v_pk_max_f16 v77, v37, 0
	v_pk_max_f16 v76, v36, 0
	v_cvt_pk_f16_f32 v36, v80, v81
	s_waitcnt vmcnt(0) lgkmcnt(12)
	v_mfma_f32_32x32x16_f16 v[48:63], v[40:43], v[20:23], v[48:63]
	v_cvt_pk_f16_f32 v38, v84, v85
	v_cvt_pk_f16_f32 v39, v86, v87
	ds_read_b128 v[84:87], v255 offset:5120
	v_cvt_pk_f16_f32 v37, v82, v83
	v_pk_max_f16 v80, v36, 0
	v_cvt_pk_f16_f32 v36, v92, v93
	s_mov_b32 s6, 0x20000
	s_waitcnt vmcnt(0) lgkmcnt(12)
	v_mfma_f32_32x32x16_f16 v[48:63], v[170:173], v[24:27], v[48:63]
	v_pk_max_f16 v83, v39, 0
	v_pk_max_f16 v81, v37, 0
	v_cvt_pk_f16_f32 v39, v90, v91
	v_cvt_pk_f16_f32 v37, v94, v95
	v_pk_max_f16 v90, v36, 0
	v_add_co_u32_e32 v36, vcc, s6, v156
	s_waitcnt vmcnt(0) lgkmcnt(10)
	v_mfma_f32_32x32x16_f16 v[48:63], v[166:169], v[64:67], v[48:63]
	v_pk_max_f16 v82, v38, 0
	v_pk_max_f16 v91, v37, 0
	v_addc_co_u32_e32 v37, vcc, 0, v157, vcc
	ds_read_b128 v[92:95], v255 offset:7168
	v_cvt_pk_f16_f32 v207, v44, v45
	v_and_b32_e32 v190, 0x7fff7fff, v207
	v_mfma_f32_32x32x16_f16 v[48:63], v[182:185], v[76:79], v[48:63]
	ds_read_b128 v[166:169], v255 offset:10240
	v_pk_fma_f16 v44, v190, s2, v164 op_sel_hi:[1,0,0]
	v_cvt_pk_f16_f32 v38, v88, v89
	v_pk_fma_f16 v44, v44, v190, s3 op_sel_hi:[1,1,0]
	v_pk_max_f16 v88, v38, 0
	v_pk_mul_f16 v44, v190, v44
	v_pk_add_f16 v38, v159, v153
	s_waitcnt vmcnt(0) lgkmcnt(10)
	v_mfma_f32_32x32x16_f16 v[48:63], v[116:119], v[80:83], v[48:63]
	ds_read_b128 v[116:119], v255 offset:26944
	v_exp_f16_e32 v45, v44
	v_exp_f16_sdwa v36, v44 dst_sel:DWORD dst_unused:UNUSED_PAD src0_sel:WORD_1
	v_pack_b32_f16 v37, v165, v206
	v_cvt_pk_f16_f32 v155, v46, v47
	v_pk_max_f16 v89, v39, 0
	v_pk_fma_f16 v153, v159, v37, v38 neg_lo:[1,0,0] neg_hi:[1,0,0]
	v_and_b32_e32 v159, 0x7fff7fff, v155
	s_waitcnt vmcnt(0) lgkmcnt(10)
	v_mfma_f32_32x32x16_f16 v[48:63], v[124:127], v[88:91], v[48:63]
	v_pk_fma_f16 v124, v159, s2, v164 op_sel_hi:[1,0,0]
	v_pack_b32_f16 v154, v45, v36
	v_pk_fma_f16 v124, v124, v159, s3 op_sel_hi:[1,1,0]
	v_pk_add_f16 v171, v190, v207
	v_pk_mul_f16 v165, v159, v124
	ds_read_b128 v[124:127], v255 offset:11264
	v_exp_f16_e32 v170, v165
	s_waitcnt vmcnt(0) lgkmcnt(10)
	v_mfma_f32_32x32x16_f16 v[32:47], v[32:35], v[96:99], 0
	v_exp_f16_sdwa v165, v165 dst_sel:DWORD dst_unused:UNUSED_PAD src0_sel:WORD_1
	v_pk_fma_f16 v154, v190, v154, v171 neg_lo:[1,0,0] neg_hi:[1,0,0]
	s_mov_b32 s6, 0x1e000
	v_cvt_pk_f16_f32 v4, v4, v5
	v_and_b32_e32 v5, 0x7fff7fff, v4
	v_cvt_pk_f16_f32 v56, v56, v57
	v_cvt_pk_f16_f32 v57, v58, v59
	s_waitcnt vmcnt(0) lgkmcnt(9)
	v_mfma_f32_32x32x16_f16 v[32:47], v[16:19], v[174:177], v[32:47]
	v_pack_b32_f16 v16, v170, v165
	ds_read_b128 v[170:173], v255 offset:12288
	v_add_co_u32_e32 v174, vcc, s6, v156
	v_cvt_pk_f16_f32 v18, v0, v1
	s_nop 0
	v_addc_co_u32_e32 v175, vcc, 0, v157, vcc
	s_waitcnt vmcnt(0) lgkmcnt(9)
	v_mfma_f32_32x32x16_f16 v[32:47], v[132:135], v[128:131], v[32:47]
	ds_read_b128 v[128:131], v255 offset:13312
	v_and_b32_e32 v19, 0x7fff7fff, v18
	ds_read_b128 v[132:135], v255 offset:14336
	v_pk_fma_f16 v0, v19, s2, v164 op_sel_hi:[1,0,0]
	v_pk_add_f16 v17, v159, v155
	v_pk_fma_f16 v0, v0, v19, s3 op_sel_hi:[1,1,0]
	s_mov_b32 s6, 0x1d000
	v_mfma_f32_32x32x16_f16 v[32:47], v[28:31], v[20:23], v[32:47]
	v_pk_mul_f16 v0, v19, v0
	v_pk_fma_f16 v155, v159, v16, v17 neg_lo:[1,0,0] neg_hi:[1,0,0]
	v_exp_f16_e32 v1, v0
	v_exp_f16_sdwa v0, v0 dst_sel:DWORD dst_unused:UNUSED_PAD src0_sel:WORD_1
	v_add_co_u32_e32 v16, vcc, s6, v156
	v_cvt_pk_f16_f32 v20, v2, v3
	s_nop 0
	v_addc_co_u32_e32 v17, vcc, 0, v157, vcc
	v_pack_b32_f16 v159, v1, v0
	s_waitcnt vmcnt(0) lgkmcnt(10)
	v_mfma_f32_32x32x16_f16 v[32:47], v[68:71], v[24:27], v[32:47]
	ds_read_b128 v[0:3], v255 offset:15360
	v_and_b32_e32 v21, 0x7fff7fff, v20
	v_pk_fma_f16 v22, v21, s2, v164 op_sel_hi:[1,0,0]
	v_pk_add_f16 v18, v19, v18
	v_pk_fma_f16 v22, v22, v21, s3 op_sel_hi:[1,1,0]
	v_pk_fma_f16 v68, v19, v159, v18 neg_lo:[1,0,0] neg_hi:[1,0,0]
	v_pk_mul_f16 v22, v21, v22
	s_waitcnt vmcnt(0) lgkmcnt(10)
	v_mfma_f32_32x32x16_f16 v[32:47], v[72:75], v[64:67], v[32:47]
	ds_read_b128 v[64:67], v255 offset:16384
	ds_read_b128 v[72:75], v255 offset:17728
	v_pk_fma_f16 v16, v5, s2, v164 op_sel_hi:[1,0,0]
	v_cvt_pk_f16_f32 v17, v50, v51
	v_pk_fma_f16 v70, v16, v5, s3 op_sel_hi:[1,1,0]
	v_cvt_pk_f16_f32 v16, v48, v49
	ds_read_b128 v[48:51], v255 offset:18752
	s_waitcnt vmcnt(0) lgkmcnt(12)
	v_mfma_f32_32x32x16_f16 v[32:47], v[160:163], v[76:79], v[32:47]
	v_exp_f16_e32 v23, v22
	v_exp_f16_sdwa v22, v22 dst_sel:DWORD dst_unused:UNUSED_PAD src0_sel:WORD_1
	ds_read_b128 v[76:79], v255 offset:19776
	v_pk_add_f16 v19, v21, v20
	v_cvt_pk_f16_f32 v58, v60, v61
	v_pack_b32_f16 v18, v23, v22
	v_pk_fma_f16 v69, v21, v18, v19 neg_lo:[1,0,0] neg_hi:[1,0,0]
	s_waitcnt vmcnt(0) lgkmcnt(12)
	v_mfma_f32_32x32x16_f16 v[32:47], v[84:87], v[80:83], v[32:47]
	v_cvt_pk_f16_f32 v18, v52, v53
	v_cvt_pk_f16_f32 v19, v54, v55
	v_pk_max_f16 v55, v19, 0
	v_pk_max_f16 v54, v18, 0
	v_pk_max_f16 v53, v17, 0
	v_pk_max_f16 v52, v16, 0
	v_cvt_pk_f16_f32 v59, v62, v63
	s_waitcnt vmcnt(0) lgkmcnt(9)
	v_mfma_f32_32x32x16_f16 v[16:31], v[116:119], v[96:99], 0
	ds_read_b128 v[60:63], v255 offset:20800
	v_pk_max_f16 v59, v59, 0
	v_pk_max_f16 v58, v58, 0
	v_pk_max_f16 v57, v57, 0
	v_pk_max_f16 v56, v56, 0
	v_cvt_pk_f16_f32 v6, v6, v7
	v_and_b32_e32 v7, 0x7fff7fff, v6
	v_mfma_f32_32x32x16_f16 v[32:47], v[92:95], v[88:91], v[32:47]
	v_pk_add_f16 v4, v5, v4
	s_mov_b32 s6, 0x1f000
	v_mfma_f32_32x32x16_f16 v[16:31], v[166:169], v[52:55], v[16:31]
	s_nop 8
	v_cvt_pk_f16_f32 v32, v32, v33
	v_cvt_pk_f16_f32 v33, v34, v35
	v_cvt_pk_f16_f32 v34, v36, v37
	v_cvt_pk_f16_f32 v35, v38, v39
	ds_read_b128 v[36:39], v255 offset:21824
	v_pk_max_f16 v35, v35, 0
	v_pk_max_f16 v34, v34, 0
	s_waitcnt vmcnt(0) lgkmcnt(10)
	v_mfma_f32_32x32x16_f16 v[16:31], v[124:127], v[56:59], v[16:31]
	v_pk_max_f16 v33, v33, 0
	v_pk_max_f16 v32, v32, 0
	v_cvt_pk_f16_f32 v40, v40, v41
	v_add_co_u32_e32 v56, vcc, s6, v156
	s_nop 1
	v_addc_co_u32_e32 v57, vcc, 0, v157, vcc
	s_waitcnt vmcnt(0) lgkmcnt(9)
	v_mfma_f32_32x32x16_f16 v[16:31], v[170:173], v[32:35], v[16:31]
	v_cvt_pk_f16_f32 v32, v42, v43
	v_cvt_pk_f16_f32 v33, v44, v45
	v_cvt_pk_f16_f32 v34, v46, v47
	v_pk_max_f16 v35, v34, 0
	v_pk_max_f16 v34, v33, 0
	v_pk_max_f16 v33, v32, 0
	v_pk_max_f16 v32, v40, 0
	ds_read_b128 v[52:55], v255 offset:22848
	s_waitcnt vmcnt(0) lgkmcnt(9)
	v_mfma_f32_32x32x16_f16 v[16:31], v[128:131], v[32:35], v[16:31]
	v_pk_fma_f16 v34, v7, s2, v164 op_sel_hi:[1,0,0]
	v_pk_mul_f16 v32, v5, v70
	v_pk_fma_f16 v34, v34, v7, s3 op_sel_hi:[1,1,0]
	v_exp_f16_e32 v33, v32
	v_exp_f16_sdwa v32, v32 dst_sel:DWORD dst_unused:UNUSED_PAD src0_sel:WORD_1
	v_pk_mul_f16 v34, v7, v34
	v_pack_b32_f16 v32, v33, v32
	s_waitcnt vmcnt(0) lgkmcnt(8)
	v_mfma_f32_32x32x16_f16 v[16:31], v[132:135], v[120:123], v[16:31]
	v_exp_f16_e32 v35, v34
	v_exp_f16_sdwa v34, v34 dst_sel:DWORD dst_unused:UNUSED_PAD src0_sel:WORD_1
	v_pk_fma_f16 v70, v5, v32, v4 neg_lo:[1,0,0] neg_hi:[1,0,0]
	v_pack_b32_f16 v4, v35, v34
	s_waitcnt vmcnt(0) lgkmcnt(7)
	v_mfma_f32_32x32x16_f16 v[16:31], v[0:3], v[136:139], v[16:31]
	v_pk_add_f16 v0, v7, v6
	s_nop 0
	v_pk_fma_f16 v71, v7, v4, v0 neg_lo:[1,0,0] neg_hi:[1,0,0]
	v_cvt_pk_f16_f32 v0, v8, v9
	v_and_b32_e32 v1, 0x7fff7fff, v0
	v_cvt_pk_f16_f32 v4, v10, v11
	v_pk_fma_f16 v2, v1, s2, v164 op_sel_hi:[1,0,0]
	s_waitcnt vmcnt(0) lgkmcnt(6)
	v_mfma_f32_32x32x16_f16 v[16:31], v[64:67], v[140:143], v[16:31]
	v_and_b32_e32 v5, 0x7fff7fff, v4
	v_pk_fma_f16 v2, v2, v1, s3 op_sel_hi:[1,1,0]
	v_pk_fma_f16 v6, v5, s2, v164 op_sel_hi:[1,0,0]
	v_pk_mul_f16 v2, v1, v2
	v_pk_fma_f16 v6, v6, v5, s3 op_sel_hi:[1,1,0]
	v_exp_f16_e32 v3, v2
	v_exp_f16_sdwa v2, v2 dst_sel:DWORD dst_unused:UNUSED_PAD src0_sel:WORD_1
	s_waitcnt vmcnt(0) lgkmcnt(5)
	v_mfma_f32_32x32x16_f16 v[16:31], v[72:75], v[144:147], v[16:31]
	v_pk_mul_f16 v6, v5, v6
	v_pk_add_f16 v0, v1, v0
	v_exp_f16_e32 v7, v6
	v_exp_f16_sdwa v6, v6 dst_sel:DWORD dst_unused:UNUSED_PAD src0_sel:WORD_1
	v_pack_b32_f16 v2, v3, v2
	v_pk_fma_f16 v0, v1, v2, v0 neg_lo:[1,0,0] neg_hi:[1,0,0]
	v_pk_add_f16 v2, v5, v4
	s_waitcnt vmcnt(0) lgkmcnt(4)
	v_mfma_f32_32x32x16_f16 v[16:31], v[48:51], v[148:151], v[16:31]
	v_pack_b32_f16 v1, v7, v6
	v_pk_fma_f16 v1, v5, v1, v2 neg_lo:[1,0,0] neg_hi:[1,0,0]
	v_cvt_pk_f16_f32 v2, v12, v13
	v_and_b32_e32 v3, 0x7fff7fff, v2
	v_cvt_pk_f16_f32 v6, v14, v15
	v_pk_fma_f16 v4, v3, s2, v164 op_sel_hi:[1,0,0]
	v_and_b32_e32 v7, 0x7fff7fff, v6
	s_waitcnt vmcnt(0) lgkmcnt(3)
	v_mfma_f32_32x32x16_f16 v[16:31], v[76:79], v[152:155], v[16:31]
	v_pk_fma_f16 v4, v4, v3, s3 op_sel_hi:[1,1,0]
	v_pk_fma_f16 v8, v7, s2, v164 op_sel_hi:[1,0,0]
	v_pk_mul_f16 v4, v3, v4
	v_pk_fma_f16 v8, v8, v7, s3 op_sel_hi:[1,1,0]
	v_exp_f16_e32 v5, v4
	v_exp_f16_sdwa v4, v4 dst_sel:DWORD dst_unused:UNUSED_PAD src0_sel:WORD_1
	v_pk_mul_f16 v8, v7, v8
	s_waitcnt vmcnt(0) lgkmcnt(2)
	v_mfma_f32_32x32x16_f16 v[16:31], v[60:63], v[68:71], v[16:31]
	v_exp_f16_e32 v9, v8
	v_exp_f16_sdwa v8, v8 dst_sel:DWORD dst_unused:UNUSED_PAD src0_sel:WORD_1
	v_pack_b32_f16 v4, v5, v4
	v_pk_add_f16 v2, v3, v2
	s_nop 0
	v_pk_fma_f16 v2, v3, v4, v2 neg_lo:[1,0,0] neg_hi:[1,0,0]
	v_pack_b32_f16 v3, v9, v8
	v_pk_add_f16 v4, v7, v6
	s_nop 0
	v_pk_fma_f16 v3, v7, v3, v4 neg_lo:[1,0,0] neg_hi:[1,0,0]
	ds_read_b128 v[4:7], v255 offset:24896
	s_waitcnt vmcnt(0) lgkmcnt(2)
	v_mfma_f32_32x32x16_f16 v[16:31], v[36:39], v[0:3], v[16:31]
	ds_read_b128 v[0:3], v255 offset:23872
	s_waitcnt vmcnt(0) lgkmcnt(2)
	v_mfma_f32_32x32x16_f16 v[16:31], v[52:55], v[104:107], v[16:31]
	s_waitcnt vmcnt(0) lgkmcnt(0)
	v_mfma_f32_32x32x16_f16 v[16:31], v[0:3], v[100:103], v[16:31]
	ds_read_b128 v[0:3], v255 offset:25920
	v_mfma_f32_32x32x16_f16 v[16:31], v[4:7], v[112:115], v[16:31]
	s_waitcnt vmcnt(0) lgkmcnt(0)
	v_mfma_f32_32x32x16_f16 v[16:31], v[0:3], v[108:111], v[16:31]
	s_nop 11
	ds_bpermute_b32 v3, v209, v16
	ds_bpermute_b32 v2, v209, v17
	ds_bpermute_b32 v1, v209, v18
	ds_bpermute_b32 v0, v209, v19
	s_and_saveexec_b64 s[2:3], s[0:1]
	s_cbranch_execz .LBB0_33
	v_max_f32_e32 v4, v17, v17
	v_max_f32_e32 v5, v16, v16
	v_max_f32_e32 v4, v5, v4
	v_max_f32_e32 v5, v19, v19
	v_max_f32_e32 v6, v18, v18
	v_max_f32_e32 v5, v6, v5
	s_waitcnt vmcnt(0) lgkmcnt(3)
	v_max3_f32 v6, v4, v5, v3
	v_sub_f32_e32 v4, v16, v6
	v_sub_f32_e32 v5, v17, v6
	v_sub_f32_e32 v7, v18, v6
	v_mul_f32_e32 v4, 0x3fb8aa3b, v4
	v_mul_f32_e32 v5, 0x3fb8aa3b, v5
	v_mul_f32_e32 v7, 0x3fb8aa3b, v7
	v_exp_f32_e32 v4, v4
	v_exp_f32_e32 v5, v5
	v_exp_f32_e32 v9, v7
	v_sub_f32_e32 v7, v19, v6
	v_mul_f32_e32 v7, 0x3fb8aa3b, v7
	v_sub_f32_e32 v6, v3, v6
	v_exp_f32_e32 v7, v7
	v_mul_f32_e32 v6, 0x3fb8aa3b, v6
	v_exp_f32_e32 v6, v6
	v_add_f32_e32 v8, v4, v5
	v_add_f32_e32 v8, v9, v8
	v_add_f32_e32 v8, v7, v8
	v_add_f32_e32 v8, v6, v8
	v_rcp_f32_e32 v8, v8
	s_waitcnt vmcnt(0) lgkmcnt(1)
	v_mul_f32_e32 v1, 0xbfb8aa3b, v1
	v_exp_f32_e32 v1, v1
	s_mov_b32 s1, 0x403fba14
	v_pk_mul_f32 v[6:7], v[6:7], v[8:9] op_sel_hi:[1,0]
	s_mov_b32 s0, 0x40f33a98
	v_pk_mul_f32 v[20:21], v[4:5], v[8:9] op_sel_hi:[1,0]
	v_pk_mul_f32 v[14:15], v[6:7], s[0:1]
	s_mov_b32 s0, 0x411e74af
	v_add_f32_e32 v4, v20, v21
	v_mul_f32_e32 v12, v9, v8
	v_fmac_f32_e32 v4, v9, v8
	v_pk_mul_f32 v[8:9], v[20:21], s[0:1]
	s_mov_b32 s3, 0x4108466c
	s_mov_b32 s2, s1
	v_add_f32_e32 v1, 1.0, v1
	v_mul_f32_e32 v13, 0x411e74af, v6
	v_pk_fma_f32 v[8:9], v[20:21], s[2:3], v[8:9] op_sel:[0,0,1] op_sel_hi:[1,1,0]
	s_mov_b32 s2, 0x40dd0c55
	s_mov_b32 s3, s0
	v_max_f32_e32 v2, v2, v2
	v_rcp_f32_e32 v1, v1
	v_mul_f32_e32 v7, 0x40c6de12, v7
	v_pk_fma_f32 v[8:9], v[12:13], s[2:3], v[8:9] op_sel_hi:[0,1,1]
	v_mov_b32_e32 v6, v15
	v_max_f32_e32 v2, 0xc1400000, v2
	v_pk_add_f32 v[6:7], v[6:7], v[8:9]
	v_mov_b32_e32 v15, v13
	v_min_f32_e32 v2, 0x41400000, v2
	v_pk_add_f32 v[6:7], v[14:15], v[6:7]
	s_mov_b32 s4, 0xbfb8aa3b
	v_mul_f32_e32 v4, v2, v4
	v_sub_f32_e32 v2, v7, v6
	v_fmac_f32_e32 v6, v1, v2
	s_waitcnt vmcnt(0) lgkmcnt(0)
	v_mul_f32_e64 v1, |v0|, s4
	v_exp_f32_e32 v1, v1
	v_max_f32_e32 v0, v0, v0
	v_mov_b32_e32 v2, 0x411e74af
	v_max_f32_e32 v0, 0, v0
	v_add_f32_e32 v1, 1.0, v1
	v_log_f32_e32 v1, v1
	v_med3_f32 v2, v6, s1, v2
	v_mul_f32_e32 v2, 0x3fb8aa3b, v2
	v_exp_f32_e32 v5, v2
	v_fmamk_f32 v0, v1, 0x3f317218, v0
	v_add_f32_e32 v0, 0x3dcccccd, v0
	v_max_f32_e32 v0, 0x3dcccccd, v0
	v_min_f32_e32 v6, 0x41200000, v0
	v_lshlrev_b32_e32 v0, 3, v158
	v_mov_b32_e32 v10, s38
	v_mov_b32_e32 v11, s39
	v_ashrrev_i32_e32 v1, 31, v0
	v_lshl_add_u64 v[8:9], v[0:1], 2, v[10:11]
	v_mov_b32_e32 v7, v16
	v_pk_mov_b32 v[0:1], v[16:17], v[18:19] op_sel:[1,0]
	v_mov_b32_e32 v2, v19
	global_store_dwordx4 v[8:9], v[4:7], off
	global_store_dwordx4 v[8:9], v[0:3], off offset:16
